# bf16 MMA segments: compiler s_nop pads between same-accumulator MFMA pairs removed, per-register lgkm waits merged pairwise (4 instead of 8 per segment)
# speedup vs baseline: 1.0056x; 1.0056x over previous
.LBB0_216:
	s_waitcnt lgkmcnt(0)
	s_add_i32 s33, s92, 0x100
	s_add_i32 s66, s93, 0x100
	s_barrier
	s_setprio 1
	s_waitcnt lgkmcnt(6)
	v_mfma_f32_16x16x32_bf16 v[124:127], v[156:159], v[188:191], 0
	v_mfma_f32_16x16x32_bf16 v[124:127], v[152:155], v[184:187], v[124:127]
	v_mfma_f32_16x16x32_bf16 v[120:123], v[148:151], v[188:191], 0
	v_mfma_f32_16x16x32_bf16 v[120:123], v[144:147], v[184:187], v[120:123]
	s_waitcnt lgkmcnt(4)
	v_mfma_f32_16x16x32_bf16 v[116:119], v[156:159], v[180:183], 0
	v_mfma_f32_16x16x32_bf16 v[116:119], v[152:155], v[176:179], v[116:119]
	v_mfma_f32_16x16x32_bf16 v[112:115], v[148:151], v[180:183], 0
	v_mfma_f32_16x16x32_bf16 v[112:115], v[144:147], v[176:179], v[112:115]
	s_waitcnt lgkmcnt(2)
	v_mfma_f32_16x16x32_bf16 v[108:111], v[156:159], v[172:175], 0
	v_mfma_f32_16x16x32_bf16 v[108:111], v[152:155], v[168:171], v[108:111]
	v_mfma_f32_16x16x32_bf16 v[104:107], v[148:151], v[172:175], 0
	v_mfma_f32_16x16x32_bf16 v[104:107], v[144:147], v[168:171], v[104:107]
	s_waitcnt lgkmcnt(0)
	v_mfma_f32_16x16x32_bf16 v[100:103], v[156:159], v[164:167], 0
	v_mfma_f32_16x16x32_bf16 v[100:103], v[152:155], v[160:163], v[100:103]
	v_mfma_f32_16x16x32_bf16 v[96:99], v[148:151], v[164:167], 0
	v_mfma_f32_16x16x32_bf16 v[96:99], v[144:147], v[160:163], v[96:99]
	s_setprio 0
	s_setprio 1
	v_mfma_f32_16x16x32_bf16 v[92:95], v[140:143], v[188:191], 0
	v_mfma_f32_16x16x32_bf16 v[92:95], v[136:139], v[184:187], v[92:95]
	v_mfma_f32_16x16x32_bf16 v[88:91], v[132:135], v[188:191], 0
	v_mfma_f32_16x16x32_bf16 v[88:91], v[128:131], v[184:187], v[88:91]
	v_mfma_f32_16x16x32_bf16 v[84:87], v[140:143], v[180:183], 0
	v_mfma_f32_16x16x32_bf16 v[84:87], v[136:139], v[176:179], v[84:87]
	v_mfma_f32_16x16x32_bf16 v[80:83], v[132:135], v[180:183], 0
	v_mfma_f32_16x16x32_bf16 v[80:83], v[128:131], v[176:179], v[80:83]
	v_mfma_f32_16x16x32_bf16 v[76:79], v[140:143], v[172:175], 0
	v_mfma_f32_16x16x32_bf16 v[76:79], v[136:139], v[168:171], v[76:79]
	v_mfma_f32_16x16x32_bf16 v[72:75], v[132:135], v[172:175], 0
	v_mfma_f32_16x16x32_bf16 v[72:75], v[128:131], v[168:171], v[72:75]
	v_mfma_f32_16x16x32_bf16 v[68:71], v[140:143], v[164:167], 0
	v_mfma_f32_16x16x32_bf16 v[68:71], v[136:139], v[160:163], v[68:71]
	v_mfma_f32_16x16x32_bf16 v[64:67], v[132:135], v[164:167], 0
	v_mfma_f32_16x16x32_bf16 v[64:67], v[128:131], v[160:163], v[64:67]
	s_setprio 0
	s_barrier
	s_mov_b32 m0, s62
	s_mov_b32 s14, s10
	s_mov_b32 s15, s11
	buffer_load_dwordx4 v202, s[12:15], s66 offen lds
	s_add_i32 s66, s93, 0x80100
	s_mov_b32 m0, s63
	s_and_b64 vcc, exec, s[4:5]
	buffer_load_dwordx4 v202, s[12:15], s66 offen lds
	s_add_i32 s66, s93, 0x8100
	s_mov_b32 m0, s64
	s_nop 0
	buffer_load_dwordx4 v202, s[12:15], s66 offen lds
	s_add_i32 s66, s93, 0x88100
	s_mov_b32 m0, s65
	s_nop 0
	buffer_load_dwordx4 v202, s[12:15], s66 offen lds
	s_mov_b32 m0, s45
	s_add_i32 s14, s92, 0x10100
	buffer_load_dwordx4 v196, s[8:11], s33 offen lds
	s_mov_b32 m0, s68
	s_nop 0
	buffer_load_dwordx4 v196, s[8:11], s14 offen lds
	ds_read_b128 v[188:191], v219 offset:16384
	ds_read_b128 v[184:187], v219 offset:17408
	ds_read_b128 v[180:183], v219 offset:18432
	ds_read_b128 v[176:179], v219 offset:19456
	ds_read_b128 v[172:175], v219 offset:20480
	ds_read_b128 v[168:171], v219 offset:21504
	ds_read_b128 v[164:167], v219 offset:22528
	ds_read_b128 v[160:163], v219 offset:23552
	s_cbranch_vccz .LBB0_227
	s_waitcnt vmcnt(24)
	s_cbranch_execnz .LBB0_219

.LBB0_219:
	s_waitcnt lgkmcnt(0)
	s_add_i32 s4, s92, 0x180
	s_add_i32 s5, s93, 0x180
	s_barrier
	s_setprio 1
	s_waitcnt lgkmcnt(6)
	v_mfma_f32_16x16x32_bf16 v[60:63], v[156:159], v[188:191], 0
	v_mfma_f32_16x16x32_bf16 v[60:63], v[152:155], v[184:187], v[60:63]
	v_mfma_f32_16x16x32_bf16 v[56:59], v[148:151], v[188:191], 0
	v_mfma_f32_16x16x32_bf16 v[56:59], v[144:147], v[184:187], v[56:59]
	s_waitcnt lgkmcnt(4)
	v_mfma_f32_16x16x32_bf16 v[52:55], v[156:159], v[180:183], 0
	v_mfma_f32_16x16x32_bf16 v[52:55], v[152:155], v[176:179], v[52:55]
	v_mfma_f32_16x16x32_bf16 v[48:51], v[148:151], v[180:183], 0
	v_mfma_f32_16x16x32_bf16 v[48:51], v[144:147], v[176:179], v[48:51]
	s_waitcnt lgkmcnt(2)
	v_mfma_f32_16x16x32_bf16 v[44:47], v[156:159], v[172:175], 0
	v_mfma_f32_16x16x32_bf16 v[44:47], v[152:155], v[168:171], v[44:47]
	v_mfma_f32_16x16x32_bf16 v[40:43], v[148:151], v[172:175], 0
	v_mfma_f32_16x16x32_bf16 v[40:43], v[144:147], v[168:171], v[40:43]
	s_waitcnt lgkmcnt(0)
	v_mfma_f32_16x16x32_bf16 v[36:39], v[156:159], v[164:167], 0
	v_mfma_f32_16x16x32_bf16 v[36:39], v[152:155], v[160:163], v[36:39]
	v_mfma_f32_16x16x32_bf16 v[32:35], v[148:151], v[164:167], 0
	v_mfma_f32_16x16x32_bf16 v[32:35], v[144:147], v[160:163], v[32:35]
	s_setprio 0
	s_setprio 1
	v_mfma_f32_16x16x32_bf16 v[28:31], v[140:143], v[188:191], 0
	v_mfma_f32_16x16x32_bf16 v[28:31], v[136:139], v[184:187], v[28:31]
	v_mfma_f32_16x16x32_bf16 v[24:27], v[132:135], v[188:191], 0
	v_mfma_f32_16x16x32_bf16 v[24:27], v[128:131], v[184:187], v[24:27]
	v_mfma_f32_16x16x32_bf16 v[20:23], v[140:143], v[180:183], 0
	v_mfma_f32_16x16x32_bf16 v[20:23], v[136:139], v[176:179], v[20:23]
	v_mfma_f32_16x16x32_bf16 v[16:19], v[132:135], v[180:183], 0
	v_mfma_f32_16x16x32_bf16 v[16:19], v[128:131], v[176:179], v[16:19]
	v_mfma_f32_16x16x32_bf16 v[12:15], v[140:143], v[172:175], 0
	v_mfma_f32_16x16x32_bf16 v[12:15], v[136:139], v[168:171], v[12:15]
	v_mfma_f32_16x16x32_bf16 v[8:11], v[132:135], v[172:175], 0
	v_mfma_f32_16x16x32_bf16 v[8:11], v[128:131], v[168:171], v[8:11]
	v_mfma_f32_16x16x32_bf16 v[4:7], v[140:143], v[164:167], 0
	v_mfma_f32_16x16x32_bf16 v[4:7], v[136:139], v[160:163], v[4:7]
	v_mfma_f32_16x16x32_bf16 v[0:3], v[132:135], v[164:167], 0
	v_mfma_f32_16x16x32_bf16 v[0:3], v[128:131], v[160:163], v[0:3]
	s_setprio 0
	s_barrier
	ds_read_b128 v[156:159], v211
	ds_read_b128 v[152:155], v212
	ds_read_b128 v[148:151], v213
	ds_read_b128 v[144:147], v214
	ds_read_b128 v[140:143], v215
	ds_read_b128 v[136:139], v216
	ds_read_b128 v[132:135], v217
	ds_read_b128 v[128:131], v218
	ds_read_b128 v[160:163], v219 offset:32768
	ds_read_b128 v[164:167], v219 offset:33792
	ds_read_b128 v[168:171], v219 offset:34816
	ds_read_b128 v[172:175], v219 offset:35840
	ds_read_b128 v[176:179], v219 offset:36864
	ds_read_b128 v[180:183], v219 offset:37888
	ds_read_b128 v[184:187], v219 offset:38912
	ds_read_b128 v[188:191], v219 offset:39936
	s_mov_b32 m0, s69
	s_add_i32 s14, s92, 0x20100
	buffer_load_dwordx4 v196, s[8:11], s14 offen lds
	s_add_i32 s14, s92, 0x30100
	s_mov_b32 m0, s70
	s_nop 0
	buffer_load_dwordx4 v196, s[8:11], s14 offen lds
	s_waitcnt vmcnt(8)
	s_waitcnt lgkmcnt(8)
	s_barrier
	s_setprio 1
	s_waitcnt lgkmcnt(6)
	v_mfma_f32_16x16x32_bf16 v[124:127], v[156:159], v[160:163], v[124:127]
	v_mfma_f32_16x16x32_bf16 v[124:127], v[152:155], v[164:167], v[124:127]
	v_mfma_f32_16x16x32_bf16 v[120:123], v[148:151], v[160:163], v[120:123]
	v_mfma_f32_16x16x32_bf16 v[120:123], v[144:147], v[164:167], v[120:123]
	s_waitcnt lgkmcnt(4)
	v_mfma_f32_16x16x32_bf16 v[116:119], v[156:159], v[168:171], v[116:119]
	v_mfma_f32_16x16x32_bf16 v[116:119], v[152:155], v[172:175], v[116:119]
	v_mfma_f32_16x16x32_bf16 v[112:115], v[148:151], v[168:171], v[112:115]
	v_mfma_f32_16x16x32_bf16 v[112:115], v[144:147], v[172:175], v[112:115]
	s_waitcnt lgkmcnt(2)
	v_mfma_f32_16x16x32_bf16 v[108:111], v[156:159], v[176:179], v[108:111]
	v_mfma_f32_16x16x32_bf16 v[108:111], v[152:155], v[180:183], v[108:111]
	v_mfma_f32_16x16x32_bf16 v[104:107], v[148:151], v[176:179], v[104:107]
	v_mfma_f32_16x16x32_bf16 v[104:107], v[144:147], v[180:183], v[104:107]
	s_waitcnt lgkmcnt(0)
	v_mfma_f32_16x16x32_bf16 v[100:103], v[156:159], v[184:187], v[100:103]
	v_mfma_f32_16x16x32_bf16 v[100:103], v[152:155], v[188:191], v[100:103]
	v_mfma_f32_16x16x32_bf16 v[96:99], v[148:151], v[184:187], v[96:99]
	v_mfma_f32_16x16x32_bf16 v[96:99], v[144:147], v[188:191], v[96:99]
	s_setprio 0
	s_setprio 1
	v_mfma_f32_16x16x32_bf16 v[92:95], v[140:143], v[160:163], v[92:95]
	v_mfma_f32_16x16x32_bf16 v[92:95], v[136:139], v[164:167], v[92:95]
	v_mfma_f32_16x16x32_bf16 v[88:91], v[132:135], v[160:163], v[88:91]
	v_mfma_f32_16x16x32_bf16 v[88:91], v[128:131], v[164:167], v[88:91]
	v_mfma_f32_16x16x32_bf16 v[84:87], v[140:143], v[168:171], v[84:87]
	v_mfma_f32_16x16x32_bf16 v[84:87], v[136:139], v[172:175], v[84:87]
	v_mfma_f32_16x16x32_bf16 v[80:83], v[132:135], v[168:171], v[80:83]
	v_mfma_f32_16x16x32_bf16 v[80:83], v[128:131], v[172:175], v[80:83]
	v_mfma_f32_16x16x32_bf16 v[76:79], v[140:143], v[176:179], v[76:79]
	v_mfma_f32_16x16x32_bf16 v[76:79], v[136:139], v[180:183], v[76:79]
	v_mfma_f32_16x16x32_bf16 v[72:75], v[132:135], v[176:179], v[72:75]
	v_mfma_f32_16x16x32_bf16 v[72:75], v[128:131], v[180:183], v[72:75]
	v_mfma_f32_16x16x32_bf16 v[68:71], v[140:143], v[184:187], v[68:71]
	v_mfma_f32_16x16x32_bf16 v[68:71], v[136:139], v[188:191], v[68:71]
	v_mfma_f32_16x16x32_bf16 v[64:67], v[132:135], v[184:187], v[64:67]
	v_mfma_f32_16x16x32_bf16 v[64:67], v[128:131], v[188:191], v[64:67]
	s_setprio 0
	s_barrier
	ds_read_b128 v[160:163], v219 offset:49152
	ds_read_b128 v[164:167], v219 offset:50176
	ds_read_b128 v[168:171], v219 offset:51200
	ds_read_b128 v[172:175], v219 offset:52224
	ds_read_b128 v[176:179], v219 offset:53248
	ds_read_b128 v[180:183], v219 offset:54272
	ds_read_b128 v[184:187], v219 offset:55296
	ds_read_b128 v[188:191], v219 offset:56320
	s_mov_b32 m0, s73
	s_mov_b32 s14, s10
	s_mov_b32 s15, s11
	buffer_load_dwordx4 v202, s[12:15], s5 offen lds
	s_add_i32 s5, s93, 0x80180
	s_mov_b32 m0, s74
	s_nop 0
	buffer_load_dwordx4 v202, s[12:15], s5 offen lds
	s_add_i32 s5, s93, 0x8180
	s_mov_b32 m0, s77
	s_nop 0
	buffer_load_dwordx4 v202, s[12:15], s5 offen lds
	s_add_i32 s5, s93, 0x88180
	s_mov_b32 m0, s78
	s_nop 0
	buffer_load_dwordx4 v202, s[12:15], s5 offen lds
	s_mov_b32 m0, s75
	s_nop 0
	buffer_load_dwordx4 v196, s[8:11], s4 offen lds
	s_add_i32 s4, s92, 0x10180
	s_mov_b32 m0, s76
	s_nop 0
	buffer_load_dwordx4 v196, s[8:11], s4 offen lds
	s_waitcnt vmcnt(8)
	s_waitcnt lgkmcnt(6)
	s_barrier
	s_setprio 1
	s_waitcnt lgkmcnt(6)
	v_mfma_f32_16x16x32_bf16 v[60:63], v[156:159], v[160:163], v[60:63]
	v_mfma_f32_16x16x32_bf16 v[60:63], v[152:155], v[164:167], v[60:63]
	v_mfma_f32_16x16x32_bf16 v[56:59], v[148:151], v[160:163], v[56:59]
	v_mfma_f32_16x16x32_bf16 v[56:59], v[144:147], v[164:167], v[56:59]
	s_waitcnt lgkmcnt(4)
	v_mfma_f32_16x16x32_bf16 v[52:55], v[156:159], v[168:171], v[52:55]
	v_mfma_f32_16x16x32_bf16 v[52:55], v[152:155], v[172:175], v[52:55]
	v_mfma_f32_16x16x32_bf16 v[48:51], v[148:151], v[168:171], v[48:51]
	v_mfma_f32_16x16x32_bf16 v[48:51], v[144:147], v[172:175], v[48:51]
	s_waitcnt lgkmcnt(2)
	v_mfma_f32_16x16x32_bf16 v[44:47], v[156:159], v[176:179], v[44:47]
	v_mfma_f32_16x16x32_bf16 v[44:47], v[152:155], v[180:183], v[44:47]
	v_mfma_f32_16x16x32_bf16 v[40:43], v[148:151], v[176:179], v[40:43]
	v_mfma_f32_16x16x32_bf16 v[40:43], v[144:147], v[180:183], v[40:43]
	s_waitcnt lgkmcnt(0)
	v_mfma_f32_16x16x32_bf16 v[36:39], v[156:159], v[184:187], v[36:39]
	v_mfma_f32_16x16x32_bf16 v[36:39], v[152:155], v[188:191], v[36:39]
	v_mfma_f32_16x16x32_bf16 v[32:35], v[148:151], v[184:187], v[32:35]
	v_mfma_f32_16x16x32_bf16 v[32:35], v[144:147], v[188:191], v[32:35]
	s_setprio 0
	s_setprio 1
	v_mfma_f32_16x16x32_bf16 v[28:31], v[140:143], v[160:163], v[28:31]
	v_mfma_f32_16x16x32_bf16 v[28:31], v[136:139], v[164:167], v[28:31]
	v_mfma_f32_16x16x32_bf16 v[24:27], v[132:135], v[160:163], v[24:27]
	v_mfma_f32_16x16x32_bf16 v[24:27], v[128:131], v[164:167], v[24:27]
	v_mfma_f32_16x16x32_bf16 v[20:23], v[140:143], v[168:171], v[20:23]
	v_mfma_f32_16x16x32_bf16 v[20:23], v[136:139], v[172:175], v[20:23]
	v_mfma_f32_16x16x32_bf16 v[16:19], v[132:135], v[168:171], v[16:19]
	v_mfma_f32_16x16x32_bf16 v[16:19], v[128:131], v[172:175], v[16:19]
	v_mfma_f32_16x16x32_bf16 v[12:15], v[140:143], v[176:179], v[12:15]
	v_mfma_f32_16x16x32_bf16 v[12:15], v[136:139], v[180:183], v[12:15]
	v_mfma_f32_16x16x32_bf16 v[8:11], v[132:135], v[176:179], v[8:11]
	v_mfma_f32_16x16x32_bf16 v[8:11], v[128:131], v[180:183], v[8:11]
	v_mfma_f32_16x16x32_bf16 v[4:7], v[140:143], v[184:187], v[4:7]
	v_mfma_f32_16x16x32_bf16 v[4:7], v[136:139], v[188:191], v[4:7]
	v_mfma_f32_16x16x32_bf16 v[0:3], v[132:135], v[184:187], v[0:3]
	v_mfma_f32_16x16x32_bf16 v[0:3], v[128:131], v[188:191], v[0:3]
	s_setprio 0
	s_barrier
	s_add_i32 s4, s92, 0x30180
	s_add_i32 s5, s93, 0x200
	s_mov_b32 s33, 0
.LBB0_220:
	ds_read_b128 v[128:131], v203
	ds_read_b128 v[132:135], v204
	ds_read_b128 v[136:139], v205
	ds_read_b128 v[140:143], v206
	ds_read_b128 v[144:147], v207
	ds_read_b128 v[148:151], v208
	ds_read_b128 v[152:155], v209
	ds_read_b128 v[156:159], v210
	ds_read_b128 v[160:163], v219
	ds_read_b128 v[164:167], v219 offset:1024
	ds_read_b128 v[168:171], v219 offset:2048
	ds_read_b128 v[172:175], v219 offset:3072
	ds_read_b128 v[176:179], v219 offset:4096
	ds_read_b128 v[180:183], v219 offset:5120
	ds_read_b128 v[184:187], v219 offset:6144
	ds_read_b128 v[188:191], v219 offset:7168
	s_add_i32 s66, s4, 0xfffd0080
	s_cmp_eq_u32 s33, 4
	s_cselect_b32 s66, s90, s66
	s_cselect_b32 s92, s91, s5
	s_add_i32 s67, s66, 0x80
	s_mov_b32 m0, s79
	s_add_i32 s93, s4, 0xffff0000
	buffer_load_dwordx4 v196, s[8:11], s93 offen lds
	s_mov_b32 m0, s81
	s_nop 0
	buffer_load_dwordx4 v196, s[8:11], s4 offen lds
	s_waitcnt vmcnt(8)
	s_waitcnt lgkmcnt(8)
	s_barrier
	s_setprio 1
	s_waitcnt lgkmcnt(6)
	v_mfma_f32_16x16x32_bf16 v[124:127], v[128:131], v[160:163], v[124:127]
	v_mfma_f32_16x16x32_bf16 v[124:127], v[132:135], v[164:167], v[124:127]
	v_mfma_f32_16x16x32_bf16 v[120:123], v[136:139], v[160:163], v[120:123]
	v_mfma_f32_16x16x32_bf16 v[120:123], v[140:143], v[164:167], v[120:123]
	s_waitcnt lgkmcnt(4)
	v_mfma_f32_16x16x32_bf16 v[116:119], v[128:131], v[168:171], v[116:119]
	v_mfma_f32_16x16x32_bf16 v[116:119], v[132:135], v[172:175], v[116:119]
	v_mfma_f32_16x16x32_bf16 v[112:115], v[136:139], v[168:171], v[112:115]
	v_mfma_f32_16x16x32_bf16 v[112:115], v[140:143], v[172:175], v[112:115]
	s_waitcnt lgkmcnt(2)
	v_mfma_f32_16x16x32_bf16 v[108:111], v[128:131], v[176:179], v[108:111]
	v_mfma_f32_16x16x32_bf16 v[108:111], v[132:135], v[180:183], v[108:111]
	v_mfma_f32_16x16x32_bf16 v[104:107], v[136:139], v[176:179], v[104:107]
	v_mfma_f32_16x16x32_bf16 v[104:107], v[140:143], v[180:183], v[104:107]
	s_waitcnt lgkmcnt(0)
	v_mfma_f32_16x16x32_bf16 v[100:103], v[128:131], v[184:187], v[100:103]
	v_mfma_f32_16x16x32_bf16 v[100:103], v[132:135], v[188:191], v[100:103]
	v_mfma_f32_16x16x32_bf16 v[96:99], v[136:139], v[184:187], v[96:99]
	v_mfma_f32_16x16x32_bf16 v[96:99], v[140:143], v[188:191], v[96:99]
	s_setprio 0
	s_setprio 1
	v_mfma_f32_16x16x32_bf16 v[92:95], v[144:147], v[160:163], v[92:95]
	v_mfma_f32_16x16x32_bf16 v[92:95], v[148:151], v[164:167], v[92:95]
	v_mfma_f32_16x16x32_bf16 v[88:91], v[152:155], v[160:163], v[88:91]
	v_mfma_f32_16x16x32_bf16 v[88:91], v[156:159], v[164:167], v[88:91]
	v_mfma_f32_16x16x32_bf16 v[84:87], v[144:147], v[168:171], v[84:87]
	v_mfma_f32_16x16x32_bf16 v[84:87], v[148:151], v[172:175], v[84:87]
	v_mfma_f32_16x16x32_bf16 v[80:83], v[152:155], v[168:171], v[80:83]
	v_mfma_f32_16x16x32_bf16 v[80:83], v[156:159], v[172:175], v[80:83]
	v_mfma_f32_16x16x32_bf16 v[76:79], v[144:147], v[176:179], v[76:79]
	v_mfma_f32_16x16x32_bf16 v[76:79], v[148:151], v[180:183], v[76:79]
	v_mfma_f32_16x16x32_bf16 v[72:75], v[152:155], v[176:179], v[72:75]
	v_mfma_f32_16x16x32_bf16 v[72:75], v[156:159], v[180:183], v[72:75]
	v_mfma_f32_16x16x32_bf16 v[68:71], v[144:147], v[184:187], v[68:71]
	v_mfma_f32_16x16x32_bf16 v[68:71], v[148:151], v[188:191], v[68:71]
	v_mfma_f32_16x16x32_bf16 v[64:67], v[152:155], v[184:187], v[64:67]
	v_mfma_f32_16x16x32_bf16 v[64:67], v[156:159], v[188:191], v[64:67]
	s_setprio 0
	s_barrier
	ds_read_b128 v[160:163], v219 offset:16384
	ds_read_b128 v[164:167], v219 offset:17408
	ds_read_b128 v[168:171], v219 offset:18432
	ds_read_b128 v[172:175], v219 offset:19456
	ds_read_b128 v[176:179], v219 offset:20480
	ds_read_b128 v[180:183], v219 offset:21504
	ds_read_b128 v[184:187], v219 offset:22528
	ds_read_b128 v[188:191], v219 offset:23552
	s_mov_b32 m0, s62
	s_add_i32 s93, s92, 0x80000
	buffer_load_dwordx4 v202, s[12:15], s92 offen lds
	s_mov_b32 m0, s63
	s_nop 0
	buffer_load_dwordx4 v202, s[12:15], s93 offen lds
	s_add_i32 s93, s92, 0x8000
	s_mov_b32 m0, s64
	s_nop 0
	buffer_load_dwordx4 v202, s[12:15], s93 offen lds
	s_add_i32 s93, s92, 0x88000
	s_mov_b32 m0, s65
	s_nop 0
	buffer_load_dwordx4 v202, s[12:15], s93 offen lds
	s_mov_b32 m0, s45
	s_add_i32 s93, s66, 0x10000
	buffer_load_dwordx4 v196, s[8:11], s66 offen lds
	s_mov_b32 m0, s68
	s_nop 0
	buffer_load_dwordx4 v196, s[8:11], s93 offen lds
	s_waitcnt vmcnt(8)
	s_waitcnt lgkmcnt(6)
	s_barrier
	s_setprio 1
	s_waitcnt lgkmcnt(6)
	v_mfma_f32_16x16x32_bf16 v[60:63], v[128:131], v[160:163], v[60:63]
	v_mfma_f32_16x16x32_bf16 v[60:63], v[132:135], v[164:167], v[60:63]
	v_mfma_f32_16x16x32_bf16 v[56:59], v[136:139], v[160:163], v[56:59]
	v_mfma_f32_16x16x32_bf16 v[56:59], v[140:143], v[164:167], v[56:59]
	s_waitcnt lgkmcnt(4)
	v_mfma_f32_16x16x32_bf16 v[52:55], v[128:131], v[168:171], v[52:55]
	v_mfma_f32_16x16x32_bf16 v[52:55], v[132:135], v[172:175], v[52:55]
	v_mfma_f32_16x16x32_bf16 v[48:51], v[136:139], v[168:171], v[48:51]
	v_mfma_f32_16x16x32_bf16 v[48:51], v[140:143], v[172:175], v[48:51]
	s_waitcnt lgkmcnt(2)
	v_mfma_f32_16x16x32_bf16 v[44:47], v[128:131], v[176:179], v[44:47]
	v_mfma_f32_16x16x32_bf16 v[44:47], v[132:135], v[180:183], v[44:47]
	v_mfma_f32_16x16x32_bf16 v[40:43], v[136:139], v[176:179], v[40:43]
	v_mfma_f32_16x16x32_bf16 v[40:43], v[140:143], v[180:183], v[40:43]
	s_waitcnt lgkmcnt(0)
	v_mfma_f32_16x16x32_bf16 v[36:39], v[128:131], v[184:187], v[36:39]
	v_mfma_f32_16x16x32_bf16 v[36:39], v[132:135], v[188:191], v[36:39]
	v_mfma_f32_16x16x32_bf16 v[32:35], v[136:139], v[184:187], v[32:35]
	v_mfma_f32_16x16x32_bf16 v[32:35], v[140:143], v[188:191], v[32:35]
	s_setprio 0
	s_setprio 1
	v_mfma_f32_16x16x32_bf16 v[28:31], v[144:147], v[160:163], v[28:31]
	v_mfma_f32_16x16x32_bf16 v[28:31], v[148:151], v[164:167], v[28:31]
	v_mfma_f32_16x16x32_bf16 v[24:27], v[152:155], v[160:163], v[24:27]
	v_mfma_f32_16x16x32_bf16 v[24:27], v[156:159], v[164:167], v[24:27]
	v_mfma_f32_16x16x32_bf16 v[20:23], v[144:147], v[168:171], v[20:23]
	v_mfma_f32_16x16x32_bf16 v[20:23], v[148:151], v[172:175], v[20:23]
	v_mfma_f32_16x16x32_bf16 v[16:19], v[152:155], v[168:171], v[16:19]
	v_mfma_f32_16x16x32_bf16 v[16:19], v[156:159], v[172:175], v[16:19]
	v_mfma_f32_16x16x32_bf16 v[12:15], v[144:147], v[176:179], v[12:15]
	v_mfma_f32_16x16x32_bf16 v[12:15], v[148:151], v[180:183], v[12:15]
	v_mfma_f32_16x16x32_bf16 v[8:11], v[152:155], v[176:179], v[8:11]
	v_mfma_f32_16x16x32_bf16 v[8:11], v[156:159], v[180:183], v[8:11]
	v_mfma_f32_16x16x32_bf16 v[4:7], v[144:147], v[184:187], v[4:7]
	v_mfma_f32_16x16x32_bf16 v[4:7], v[148:151], v[188:191], v[4:7]
	v_mfma_f32_16x16x32_bf16 v[0:3], v[152:155], v[184:187], v[0:3]
	v_mfma_f32_16x16x32_bf16 v[0:3], v[156:159], v[188:191], v[0:3]
	s_setprio 0
	s_barrier
	ds_read_b128 v[140:143], v211
	ds_read_b128 v[144:147], v212
	ds_read_b128 v[148:151], v213
	ds_read_b128 v[152:155], v214
	ds_read_b128 v[156:159], v215
	ds_read_b128 v[136:139], v216
	ds_read_b128 v[132:135], v217
	ds_read_b128 v[128:131], v218
	ds_read_b128 v[160:163], v219 offset:32768
	ds_read_b128 v[164:167], v219 offset:33792
	ds_read_b128 v[168:171], v219 offset:34816
	ds_read_b128 v[172:175], v219 offset:35840
	ds_read_b128 v[176:179], v219 offset:36864
	ds_read_b128 v[180:183], v219 offset:37888
	ds_read_b128 v[184:187], v219 offset:38912
	ds_read_b128 v[188:191], v219 offset:39936
	s_mov_b32 m0, s69
	s_add_i32 s93, s66, 0x20000
	buffer_load_dwordx4 v196, s[8:11], s93 offen lds
	s_add_i32 s93, s66, 0x30000
	s_mov_b32 m0, s70
	s_nop 0
	buffer_load_dwordx4 v196, s[8:11], s93 offen lds
	s_waitcnt vmcnt(8)
	s_waitcnt lgkmcnt(8)
	s_barrier
	s_setprio 1
	s_waitcnt lgkmcnt(6)
	v_mfma_f32_16x16x32_bf16 v[124:127], v[140:143], v[160:163], v[124:127]
	v_mfma_f32_16x16x32_bf16 v[124:127], v[144:147], v[164:167], v[124:127]
	v_mfma_f32_16x16x32_bf16 v[120:123], v[148:151], v[160:163], v[120:123]
	v_mfma_f32_16x16x32_bf16 v[120:123], v[152:155], v[164:167], v[120:123]
	s_waitcnt lgkmcnt(4)
	v_mfma_f32_16x16x32_bf16 v[116:119], v[140:143], v[168:171], v[116:119]
	v_mfma_f32_16x16x32_bf16 v[116:119], v[144:147], v[172:175], v[116:119]
	v_mfma_f32_16x16x32_bf16 v[112:115], v[148:151], v[168:171], v[112:115]
	v_mfma_f32_16x16x32_bf16 v[112:115], v[152:155], v[172:175], v[112:115]
	s_waitcnt lgkmcnt(2)
	v_mfma_f32_16x16x32_bf16 v[108:111], v[140:143], v[176:179], v[108:111]
	v_mfma_f32_16x16x32_bf16 v[108:111], v[144:147], v[180:183], v[108:111]
	v_mfma_f32_16x16x32_bf16 v[104:107], v[148:151], v[176:179], v[104:107]
	v_mfma_f32_16x16x32_bf16 v[104:107], v[152:155], v[180:183], v[104:107]
	s_waitcnt lgkmcnt(0)
	v_mfma_f32_16x16x32_bf16 v[100:103], v[140:143], v[184:187], v[100:103]
	v_mfma_f32_16x16x32_bf16 v[100:103], v[144:147], v[188:191], v[100:103]
	v_mfma_f32_16x16x32_bf16 v[96:99], v[148:151], v[184:187], v[96:99]
	v_mfma_f32_16x16x32_bf16 v[96:99], v[152:155], v[188:191], v[96:99]
	s_setprio 0
	s_setprio 1
	v_mfma_f32_16x16x32_bf16 v[92:95], v[156:159], v[160:163], v[92:95]
	v_mfma_f32_16x16x32_bf16 v[92:95], v[136:139], v[164:167], v[92:95]
	v_mfma_f32_16x16x32_bf16 v[88:91], v[132:135], v[160:163], v[88:91]
	v_mfma_f32_16x16x32_bf16 v[88:91], v[128:131], v[164:167], v[88:91]
	v_mfma_f32_16x16x32_bf16 v[84:87], v[156:159], v[168:171], v[84:87]
	v_mfma_f32_16x16x32_bf16 v[84:87], v[136:139], v[172:175], v[84:87]
	v_mfma_f32_16x16x32_bf16 v[80:83], v[132:135], v[168:171], v[80:83]
	v_mfma_f32_16x16x32_bf16 v[80:83], v[128:131], v[172:175], v[80:83]
	v_mfma_f32_16x16x32_bf16 v[76:79], v[156:159], v[176:179], v[76:79]
	v_mfma_f32_16x16x32_bf16 v[76:79], v[136:139], v[180:183], v[76:79]
	v_mfma_f32_16x16x32_bf16 v[72:75], v[132:135], v[176:179], v[72:75]
	v_mfma_f32_16x16x32_bf16 v[72:75], v[128:131], v[180:183], v[72:75]
	v_mfma_f32_16x16x32_bf16 v[68:71], v[156:159], v[184:187], v[68:71]
	v_mfma_f32_16x16x32_bf16 v[68:71], v[136:139], v[188:191], v[68:71]
	v_mfma_f32_16x16x32_bf16 v[64:67], v[132:135], v[184:187], v[64:67]
	v_mfma_f32_16x16x32_bf16 v[64:67], v[128:131], v[188:191], v[64:67]
	s_setprio 0
	s_barrier
	ds_read_b128 v[160:163], v219 offset:49152
	ds_read_b128 v[164:167], v219 offset:50176
	ds_read_b128 v[168:171], v219 offset:51200
	ds_read_b128 v[172:175], v219 offset:52224
	ds_read_b128 v[176:179], v219 offset:53248
	ds_read_b128 v[180:183], v219 offset:54272
	ds_read_b128 v[184:187], v219 offset:55296
	ds_read_b128 v[188:191], v219 offset:56320
	s_mov_b32 m0, s73
	s_add_i32 s93, s92, 0x80
	buffer_load_dwordx4 v202, s[12:15], s93 offen lds
	s_add_i32 s93, s92, 0x80080
	s_mov_b32 m0, s74
	s_add_i32 s66, s66, 0x10080
	buffer_load_dwordx4 v202, s[12:15], s93 offen lds
	s_add_i32 s93, s92, 0x8080
	s_mov_b32 m0, s77
	s_add_i32 s92, s92, 0x88080
	buffer_load_dwordx4 v202, s[12:15], s93 offen lds
	s_mov_b32 m0, s78
	s_nop 0
	buffer_load_dwordx4 v202, s[12:15], s92 offen lds
	s_mov_b32 m0, s75
	s_nop 0
	buffer_load_dwordx4 v196, s[8:11], s67 offen lds
	s_mov_b32 m0, s76
	s_nop 0
	buffer_load_dwordx4 v196, s[8:11], s66 offen lds
	s_waitcnt vmcnt(8)
	s_waitcnt lgkmcnt(6)
	s_barrier
	s_setprio 1
	s_waitcnt lgkmcnt(6)
	v_mfma_f32_16x16x32_bf16 v[60:63], v[140:143], v[160:163], v[60:63]
	v_mfma_f32_16x16x32_bf16 v[60:63], v[144:147], v[164:167], v[60:63]
	v_mfma_f32_16x16x32_bf16 v[56:59], v[148:151], v[160:163], v[56:59]
	v_mfma_f32_16x16x32_bf16 v[56:59], v[152:155], v[164:167], v[56:59]
	s_waitcnt lgkmcnt(4)
	v_mfma_f32_16x16x32_bf16 v[52:55], v[140:143], v[168:171], v[52:55]
	v_mfma_f32_16x16x32_bf16 v[52:55], v[144:147], v[172:175], v[52:55]
	v_mfma_f32_16x16x32_bf16 v[48:51], v[148:151], v[168:171], v[48:51]
	v_mfma_f32_16x16x32_bf16 v[48:51], v[152:155], v[172:175], v[48:51]
	s_waitcnt lgkmcnt(2)
	v_mfma_f32_16x16x32_bf16 v[44:47], v[140:143], v[176:179], v[44:47]
	v_mfma_f32_16x16x32_bf16 v[44:47], v[144:147], v[180:183], v[44:47]
	v_mfma_f32_16x16x32_bf16 v[40:43], v[148:151], v[176:179], v[40:43]
	v_mfma_f32_16x16x32_bf16 v[40:43], v[152:155], v[180:183], v[40:43]
	s_waitcnt lgkmcnt(0)
	v_mfma_f32_16x16x32_bf16 v[36:39], v[140:143], v[184:187], v[36:39]
	v_mfma_f32_16x16x32_bf16 v[36:39], v[144:147], v[188:191], v[36:39]
	v_mfma_f32_16x16x32_bf16 v[32:35], v[148:151], v[184:187], v[32:35]
	v_mfma_f32_16x16x32_bf16 v[32:35], v[152:155], v[188:191], v[32:35]
	s_setprio 0
	s_setprio 1
	v_mfma_f32_16x16x32_bf16 v[28:31], v[156:159], v[160:163], v[28:31]
	v_mfma_f32_16x16x32_bf16 v[28:31], v[136:139], v[164:167], v[28:31]
	v_mfma_f32_16x16x32_bf16 v[24:27], v[132:135], v[160:163], v[24:27]
	v_mfma_f32_16x16x32_bf16 v[24:27], v[128:131], v[164:167], v[24:27]
	v_mfma_f32_16x16x32_bf16 v[20:23], v[156:159], v[168:171], v[20:23]
	v_mfma_f32_16x16x32_bf16 v[20:23], v[136:139], v[172:175], v[20:23]
	v_mfma_f32_16x16x32_bf16 v[16:19], v[132:135], v[168:171], v[16:19]
	v_mfma_f32_16x16x32_bf16 v[16:19], v[128:131], v[172:175], v[16:19]
	v_mfma_f32_16x16x32_bf16 v[12:15], v[156:159], v[176:179], v[12:15]
	v_mfma_f32_16x16x32_bf16 v[12:15], v[136:139], v[180:183], v[12:15]
	v_mfma_f32_16x16x32_bf16 v[8:11], v[132:135], v[176:179], v[8:11]
	v_mfma_f32_16x16x32_bf16 v[8:11], v[128:131], v[180:183], v[8:11]
	v_mfma_f32_16x16x32_bf16 v[4:7], v[156:159], v[184:187], v[4:7]
	v_mfma_f32_16x16x32_bf16 v[4:7], v[136:139], v[188:191], v[4:7]
	v_mfma_f32_16x16x32_bf16 v[0:3], v[132:135], v[184:187], v[0:3]
	v_mfma_f32_16x16x32_bf16 v[0:3], v[128:131], v[188:191], v[0:3]
	s_setprio 0
	s_barrier
	s_add_i32 s33, s33, 2
	s_addk_i32 s4, 0x100
	s_addk_i32 s5, 0x100
	s_cmp_gt_u32 s33, 5
	s_cbranch_scc0 .LBB0_220
	s_and_b64 vcc, exec, s[16:17]
	s_cbranch_vccz .LBB0_223
	s_barrier

.LBB0_250:
	s_waitcnt lgkmcnt(0)
	s_add_i32 s33, s91, 0x100
	s_add_i32 s66, s90, 0x100
	s_barrier
	s_setprio 1
	s_waitcnt lgkmcnt(6)
	v_mfma_f32_16x16x32_bf16 v[124:127], v[156:159], v[188:191], 0
	v_mfma_f32_16x16x32_bf16 v[124:127], v[152:155], v[184:187], v[124:127]
	v_mfma_f32_16x16x32_bf16 v[120:123], v[148:151], v[188:191], 0
	v_mfma_f32_16x16x32_bf16 v[120:123], v[144:147], v[184:187], v[120:123]
	s_waitcnt lgkmcnt(4)
	v_mfma_f32_16x16x32_bf16 v[116:119], v[156:159], v[180:183], 0
	v_mfma_f32_16x16x32_bf16 v[116:119], v[152:155], v[176:179], v[116:119]
	v_mfma_f32_16x16x32_bf16 v[112:115], v[148:151], v[180:183], 0
	v_mfma_f32_16x16x32_bf16 v[112:115], v[144:147], v[176:179], v[112:115]
	s_waitcnt lgkmcnt(2)
	v_mfma_f32_16x16x32_bf16 v[108:111], v[156:159], v[172:175], 0
	v_mfma_f32_16x16x32_bf16 v[108:111], v[152:155], v[168:171], v[108:111]
	v_mfma_f32_16x16x32_bf16 v[104:107], v[148:151], v[172:175], 0
	v_mfma_f32_16x16x32_bf16 v[104:107], v[144:147], v[168:171], v[104:107]
	s_waitcnt lgkmcnt(0)
	v_mfma_f32_16x16x32_bf16 v[100:103], v[156:159], v[164:167], 0
	v_mfma_f32_16x16x32_bf16 v[100:103], v[152:155], v[160:163], v[100:103]
	v_mfma_f32_16x16x32_bf16 v[96:99], v[148:151], v[164:167], 0
	v_mfma_f32_16x16x32_bf16 v[96:99], v[144:147], v[160:163], v[96:99]
	s_setprio 0
	s_setprio 1
	v_mfma_f32_16x16x32_bf16 v[92:95], v[140:143], v[188:191], 0
	v_mfma_f32_16x16x32_bf16 v[92:95], v[136:139], v[184:187], v[92:95]
	v_mfma_f32_16x16x32_bf16 v[88:91], v[132:135], v[188:191], 0
	v_mfma_f32_16x16x32_bf16 v[88:91], v[128:131], v[184:187], v[88:91]
	v_mfma_f32_16x16x32_bf16 v[84:87], v[140:143], v[180:183], 0
	v_mfma_f32_16x16x32_bf16 v[84:87], v[136:139], v[176:179], v[84:87]
	v_mfma_f32_16x16x32_bf16 v[80:83], v[132:135], v[180:183], 0
	v_mfma_f32_16x16x32_bf16 v[80:83], v[128:131], v[176:179], v[80:83]
	v_mfma_f32_16x16x32_bf16 v[76:79], v[140:143], v[172:175], 0
	v_mfma_f32_16x16x32_bf16 v[76:79], v[136:139], v[168:171], v[76:79]
	v_mfma_f32_16x16x32_bf16 v[72:75], v[132:135], v[172:175], 0
	v_mfma_f32_16x16x32_bf16 v[72:75], v[128:131], v[168:171], v[72:75]
	v_mfma_f32_16x16x32_bf16 v[68:71], v[140:143], v[164:167], 0
	v_mfma_f32_16x16x32_bf16 v[68:71], v[136:139], v[160:163], v[68:71]
	v_mfma_f32_16x16x32_bf16 v[64:67], v[132:135], v[164:167], 0
	v_mfma_f32_16x16x32_bf16 v[64:67], v[128:131], v[160:163], v[64:67]
	s_setprio 0
	s_barrier
	s_mov_b32 m0, s62
	s_mov_b32 s10, s6
	s_mov_b32 s11, s7
	buffer_load_dwordx4 v192, s[8:11], s66 offen lds
	s_add_i32 s66, s90, 0x20100
	s_mov_b32 m0, s63
	s_and_b64 vcc, exec, s[42:43]
	buffer_load_dwordx4 v192, s[8:11], s66 offen lds
	s_add_i32 s66, s90, 0x2100
	s_mov_b32 m0, s64
	s_nop 0
	buffer_load_dwordx4 v192, s[8:11], s66 offen lds
	s_add_i32 s66, s90, 0x22100
	s_mov_b32 m0, s65
	s_nop 0
	buffer_load_dwordx4 v192, s[8:11], s66 offen lds
	s_mov_b32 m0, s47
	s_add_i32 s10, s91, 0x10100
	buffer_load_dwordx4 v196, s[4:7], s33 offen lds
	s_mov_b32 m0, s68
	s_nop 0
	buffer_load_dwordx4 v196, s[4:7], s10 offen lds
	ds_read_b128 v[188:191], v197 offset:16384
	ds_read_b128 v[184:187], v197 offset:17408
	ds_read_b128 v[180:183], v197 offset:18432
	ds_read_b128 v[176:179], v197 offset:19456
	ds_read_b128 v[172:175], v197 offset:20480
	ds_read_b128 v[168:171], v197 offset:21504
	ds_read_b128 v[164:167], v197 offset:22528
	ds_read_b128 v[160:163], v197 offset:23552
	s_cbranch_vccz .LBB0_261
	s_waitcnt vmcnt(24)
	s_cbranch_execnz .LBB0_253

.LBB0_253:
	s_waitcnt lgkmcnt(0)
	s_add_i32 s33, s91, 0x180
	s_add_i32 s42, s90, 0x180
	s_barrier
	s_setprio 1
	s_waitcnt lgkmcnt(6)
	v_mfma_f32_16x16x32_bf16 v[60:63], v[156:159], v[188:191], 0
	v_mfma_f32_16x16x32_bf16 v[60:63], v[152:155], v[184:187], v[60:63]
	v_mfma_f32_16x16x32_bf16 v[56:59], v[148:151], v[188:191], 0
	v_mfma_f32_16x16x32_bf16 v[56:59], v[144:147], v[184:187], v[56:59]
	s_waitcnt lgkmcnt(4)
	v_mfma_f32_16x16x32_bf16 v[52:55], v[156:159], v[180:183], 0
	v_mfma_f32_16x16x32_bf16 v[52:55], v[152:155], v[176:179], v[52:55]
	v_mfma_f32_16x16x32_bf16 v[48:51], v[148:151], v[180:183], 0
	v_mfma_f32_16x16x32_bf16 v[48:51], v[144:147], v[176:179], v[48:51]
	s_waitcnt lgkmcnt(2)
	v_mfma_f32_16x16x32_bf16 v[44:47], v[156:159], v[172:175], 0
	v_mfma_f32_16x16x32_bf16 v[44:47], v[152:155], v[168:171], v[44:47]
	v_mfma_f32_16x16x32_bf16 v[40:43], v[148:151], v[172:175], 0
	v_mfma_f32_16x16x32_bf16 v[40:43], v[144:147], v[168:171], v[40:43]
	s_waitcnt lgkmcnt(0)
	v_mfma_f32_16x16x32_bf16 v[36:39], v[156:159], v[164:167], 0
	v_mfma_f32_16x16x32_bf16 v[36:39], v[152:155], v[160:163], v[36:39]
	v_mfma_f32_16x16x32_bf16 v[32:35], v[148:151], v[164:167], 0
	v_mfma_f32_16x16x32_bf16 v[32:35], v[144:147], v[160:163], v[32:35]
	s_setprio 0
	s_setprio 1
	v_mfma_f32_16x16x32_bf16 v[28:31], v[140:143], v[188:191], 0
	v_mfma_f32_16x16x32_bf16 v[28:31], v[136:139], v[184:187], v[28:31]
	v_mfma_f32_16x16x32_bf16 v[24:27], v[132:135], v[188:191], 0
	v_mfma_f32_16x16x32_bf16 v[24:27], v[128:131], v[184:187], v[24:27]
	v_mfma_f32_16x16x32_bf16 v[20:23], v[140:143], v[180:183], 0
	v_mfma_f32_16x16x32_bf16 v[20:23], v[136:139], v[176:179], v[20:23]
	v_mfma_f32_16x16x32_bf16 v[16:19], v[132:135], v[180:183], 0
	v_mfma_f32_16x16x32_bf16 v[16:19], v[128:131], v[176:179], v[16:19]
	v_mfma_f32_16x16x32_bf16 v[12:15], v[140:143], v[172:175], 0
	v_mfma_f32_16x16x32_bf16 v[12:15], v[136:139], v[168:171], v[12:15]
	v_mfma_f32_16x16x32_bf16 v[8:11], v[132:135], v[172:175], 0
	v_mfma_f32_16x16x32_bf16 v[8:11], v[128:131], v[168:171], v[8:11]
	v_mfma_f32_16x16x32_bf16 v[4:7], v[140:143], v[164:167], 0
	v_mfma_f32_16x16x32_bf16 v[4:7], v[136:139], v[160:163], v[4:7]
	v_mfma_f32_16x16x32_bf16 v[0:3], v[132:135], v[164:167], 0
	v_mfma_f32_16x16x32_bf16 v[0:3], v[128:131], v[160:163], v[0:3]
	s_setprio 0
	s_barrier
	ds_read_b128 v[156:159], v203
	ds_read_b128 v[152:155], v204
	ds_read_b128 v[148:151], v205
	ds_read_b128 v[144:147], v206
	ds_read_b128 v[140:143], v207
	ds_read_b128 v[136:139], v208
	ds_read_b128 v[132:135], v209
	ds_read_b128 v[128:131], v210
	ds_read_b128 v[160:163], v197 offset:32768
	ds_read_b128 v[164:167], v197 offset:33792
	ds_read_b128 v[168:171], v197 offset:34816
	ds_read_b128 v[172:175], v197 offset:35840
	ds_read_b128 v[176:179], v197 offset:36864
	ds_read_b128 v[180:183], v197 offset:37888
	ds_read_b128 v[184:187], v197 offset:38912
	ds_read_b128 v[188:191], v197 offset:39936
	s_mov_b32 m0, s69
	s_add_i32 s10, s91, 0x20100
	buffer_load_dwordx4 v196, s[4:7], s10 offen lds
	s_add_i32 s10, s91, 0x30100
	s_mov_b32 m0, s70
	s_nop 0
	buffer_load_dwordx4 v196, s[4:7], s10 offen lds
	s_waitcnt vmcnt(8)
	s_waitcnt lgkmcnt(8)
	s_barrier
	s_setprio 1
	s_waitcnt lgkmcnt(6)
	v_mfma_f32_16x16x32_bf16 v[124:127], v[156:159], v[160:163], v[124:127]
	v_mfma_f32_16x16x32_bf16 v[124:127], v[152:155], v[164:167], v[124:127]
	v_mfma_f32_16x16x32_bf16 v[120:123], v[148:151], v[160:163], v[120:123]
	v_mfma_f32_16x16x32_bf16 v[120:123], v[144:147], v[164:167], v[120:123]
	s_waitcnt lgkmcnt(4)
	v_mfma_f32_16x16x32_bf16 v[116:119], v[156:159], v[168:171], v[116:119]
	v_mfma_f32_16x16x32_bf16 v[116:119], v[152:155], v[172:175], v[116:119]
	v_mfma_f32_16x16x32_bf16 v[112:115], v[148:151], v[168:171], v[112:115]
	v_mfma_f32_16x16x32_bf16 v[112:115], v[144:147], v[172:175], v[112:115]
	s_waitcnt lgkmcnt(2)
	v_mfma_f32_16x16x32_bf16 v[108:111], v[156:159], v[176:179], v[108:111]
	v_mfma_f32_16x16x32_bf16 v[108:111], v[152:155], v[180:183], v[108:111]
	v_mfma_f32_16x16x32_bf16 v[104:107], v[148:151], v[176:179], v[104:107]
	v_mfma_f32_16x16x32_bf16 v[104:107], v[144:147], v[180:183], v[104:107]
	s_waitcnt lgkmcnt(0)
	v_mfma_f32_16x16x32_bf16 v[100:103], v[156:159], v[184:187], v[100:103]
	v_mfma_f32_16x16x32_bf16 v[100:103], v[152:155], v[188:191], v[100:103]
	v_mfma_f32_16x16x32_bf16 v[96:99], v[148:151], v[184:187], v[96:99]
	v_mfma_f32_16x16x32_bf16 v[96:99], v[144:147], v[188:191], v[96:99]
	s_setprio 0
	s_setprio 1
	v_mfma_f32_16x16x32_bf16 v[92:95], v[140:143], v[160:163], v[92:95]
	v_mfma_f32_16x16x32_bf16 v[92:95], v[136:139], v[164:167], v[92:95]
	v_mfma_f32_16x16x32_bf16 v[88:91], v[132:135], v[160:163], v[88:91]
	v_mfma_f32_16x16x32_bf16 v[88:91], v[128:131], v[164:167], v[88:91]
	v_mfma_f32_16x16x32_bf16 v[84:87], v[140:143], v[168:171], v[84:87]
	v_mfma_f32_16x16x32_bf16 v[84:87], v[136:139], v[172:175], v[84:87]
	v_mfma_f32_16x16x32_bf16 v[80:83], v[132:135], v[168:171], v[80:83]
	v_mfma_f32_16x16x32_bf16 v[80:83], v[128:131], v[172:175], v[80:83]
	v_mfma_f32_16x16x32_bf16 v[76:79], v[140:143], v[176:179], v[76:79]
	v_mfma_f32_16x16x32_bf16 v[76:79], v[136:139], v[180:183], v[76:79]
	v_mfma_f32_16x16x32_bf16 v[72:75], v[132:135], v[176:179], v[72:75]
	v_mfma_f32_16x16x32_bf16 v[72:75], v[128:131], v[180:183], v[72:75]
	v_mfma_f32_16x16x32_bf16 v[68:71], v[140:143], v[184:187], v[68:71]
	v_mfma_f32_16x16x32_bf16 v[68:71], v[136:139], v[188:191], v[68:71]
	v_mfma_f32_16x16x32_bf16 v[64:67], v[132:135], v[184:187], v[64:67]
	v_mfma_f32_16x16x32_bf16 v[64:67], v[128:131], v[188:191], v[64:67]
	s_setprio 0
	s_barrier
	ds_read_b128 v[160:163], v197 offset:49152
	ds_read_b128 v[164:167], v197 offset:50176
	ds_read_b128 v[168:171], v197 offset:51200
	ds_read_b128 v[172:175], v197 offset:52224
	ds_read_b128 v[176:179], v197 offset:53248
	ds_read_b128 v[180:183], v197 offset:54272
	ds_read_b128 v[184:187], v197 offset:55296
	ds_read_b128 v[188:191], v197 offset:56320
	s_mov_b32 m0, s72
	s_mov_b32 s10, s6
	s_mov_b32 s11, s7
	buffer_load_dwordx4 v192, s[8:11], s42 offen lds
	s_add_i32 s42, s90, 0x20180
	s_mov_b32 m0, s73
	s_nop 0
	buffer_load_dwordx4 v192, s[8:11], s42 offen lds
	s_add_i32 s42, s90, 0x2180
	s_mov_b32 m0, s76
	s_nop 0
	buffer_load_dwordx4 v192, s[8:11], s42 offen lds
	s_add_i32 s42, s90, 0x22180
	s_mov_b32 m0, s77
	s_nop 0
	buffer_load_dwordx4 v192, s[8:11], s42 offen lds
	s_mov_b32 m0, s74
	s_nop 0
	buffer_load_dwordx4 v196, s[4:7], s33 offen lds
	s_add_i32 s33, s91, 0x10180
	s_mov_b32 m0, s75
	s_nop 0
	buffer_load_dwordx4 v196, s[4:7], s33 offen lds
	s_waitcnt vmcnt(8)
	s_waitcnt lgkmcnt(6)
	s_barrier
	s_setprio 1
	s_waitcnt lgkmcnt(6)
	v_mfma_f32_16x16x32_bf16 v[60:63], v[156:159], v[160:163], v[60:63]
	v_mfma_f32_16x16x32_bf16 v[60:63], v[152:155], v[164:167], v[60:63]
	v_mfma_f32_16x16x32_bf16 v[56:59], v[148:151], v[160:163], v[56:59]
	v_mfma_f32_16x16x32_bf16 v[56:59], v[144:147], v[164:167], v[56:59]
	s_waitcnt lgkmcnt(4)
	v_mfma_f32_16x16x32_bf16 v[52:55], v[156:159], v[168:171], v[52:55]
	v_mfma_f32_16x16x32_bf16 v[52:55], v[152:155], v[172:175], v[52:55]
	v_mfma_f32_16x16x32_bf16 v[48:51], v[148:151], v[168:171], v[48:51]
	v_mfma_f32_16x16x32_bf16 v[48:51], v[144:147], v[172:175], v[48:51]
	s_waitcnt lgkmcnt(2)
	v_mfma_f32_16x16x32_bf16 v[44:47], v[156:159], v[176:179], v[44:47]
	v_mfma_f32_16x16x32_bf16 v[44:47], v[152:155], v[180:183], v[44:47]
	v_mfma_f32_16x16x32_bf16 v[40:43], v[148:151], v[176:179], v[40:43]
	v_mfma_f32_16x16x32_bf16 v[40:43], v[144:147], v[180:183], v[40:43]
	s_waitcnt lgkmcnt(0)
	v_mfma_f32_16x16x32_bf16 v[36:39], v[156:159], v[184:187], v[36:39]
	v_mfma_f32_16x16x32_bf16 v[36:39], v[152:155], v[188:191], v[36:39]
	v_mfma_f32_16x16x32_bf16 v[32:35], v[148:151], v[184:187], v[32:35]
	v_mfma_f32_16x16x32_bf16 v[32:35], v[144:147], v[188:191], v[32:35]
	s_setprio 0
	s_setprio 1
	v_mfma_f32_16x16x32_bf16 v[28:31], v[140:143], v[160:163], v[28:31]
	v_mfma_f32_16x16x32_bf16 v[28:31], v[136:139], v[164:167], v[28:31]
	v_mfma_f32_16x16x32_bf16 v[24:27], v[132:135], v[160:163], v[24:27]
	v_mfma_f32_16x16x32_bf16 v[24:27], v[128:131], v[164:167], v[24:27]
	v_mfma_f32_16x16x32_bf16 v[20:23], v[140:143], v[168:171], v[20:23]
	v_mfma_f32_16x16x32_bf16 v[20:23], v[136:139], v[172:175], v[20:23]
	v_mfma_f32_16x16x32_bf16 v[16:19], v[132:135], v[168:171], v[16:19]
	v_mfma_f32_16x16x32_bf16 v[16:19], v[128:131], v[172:175], v[16:19]
	v_mfma_f32_16x16x32_bf16 v[12:15], v[140:143], v[176:179], v[12:15]
	v_mfma_f32_16x16x32_bf16 v[12:15], v[136:139], v[180:183], v[12:15]
	v_mfma_f32_16x16x32_bf16 v[8:11], v[132:135], v[176:179], v[8:11]
	v_mfma_f32_16x16x32_bf16 v[8:11], v[128:131], v[180:183], v[8:11]
	v_mfma_f32_16x16x32_bf16 v[4:7], v[140:143], v[184:187], v[4:7]
	v_mfma_f32_16x16x32_bf16 v[4:7], v[136:139], v[188:191], v[4:7]
	v_mfma_f32_16x16x32_bf16 v[0:3], v[132:135], v[184:187], v[0:3]
	v_mfma_f32_16x16x32_bf16 v[0:3], v[128:131], v[188:191], v[0:3]
	s_setprio 0
	s_barrier
	s_add_i32 s33, s91, 0x30180
	s_add_i32 s42, s90, 0x200
	s_mov_b32 s43, 0
.LBB0_254:
	ds_read_b128 v[128:131], v193
	ds_read_b128 v[132:135], v194
	ds_read_b128 v[136:139], v195
	ds_read_b128 v[140:143], v198
	ds_read_b128 v[144:147], v199
	ds_read_b128 v[148:151], v200
	ds_read_b128 v[152:155], v201
	ds_read_b128 v[156:159], v202
	ds_read_b128 v[160:163], v197
	ds_read_b128 v[164:167], v197 offset:1024
	ds_read_b128 v[168:171], v197 offset:2048
	ds_read_b128 v[172:175], v197 offset:3072
	ds_read_b128 v[176:179], v197 offset:4096
	ds_read_b128 v[180:183], v197 offset:5120
	ds_read_b128 v[184:187], v197 offset:6144
	ds_read_b128 v[188:191], v197 offset:7168
	s_add_i32 s66, s33, 0xfffd0080
	s_cmp_eq_u32 s43, 4
	s_cselect_b32 s66, s88, s66
	s_cselect_b32 s90, s89, s42
	s_add_i32 s67, s66, 0x80
	s_mov_b32 m0, s78
	s_add_i32 s91, s33, 0xffff0000
	buffer_load_dwordx4 v196, s[4:7], s91 offen lds
	s_mov_b32 m0, s79
	s_nop 0
	buffer_load_dwordx4 v196, s[4:7], s33 offen lds
	s_waitcnt vmcnt(8)
	s_waitcnt lgkmcnt(8)
	s_barrier
	s_setprio 1
	s_waitcnt lgkmcnt(6)
	v_mfma_f32_16x16x32_bf16 v[124:127], v[128:131], v[160:163], v[124:127]
	v_mfma_f32_16x16x32_bf16 v[124:127], v[132:135], v[164:167], v[124:127]
	v_mfma_f32_16x16x32_bf16 v[120:123], v[136:139], v[160:163], v[120:123]
	v_mfma_f32_16x16x32_bf16 v[120:123], v[140:143], v[164:167], v[120:123]
	s_waitcnt lgkmcnt(4)
	v_mfma_f32_16x16x32_bf16 v[116:119], v[128:131], v[168:171], v[116:119]
	v_mfma_f32_16x16x32_bf16 v[116:119], v[132:135], v[172:175], v[116:119]
	v_mfma_f32_16x16x32_bf16 v[112:115], v[136:139], v[168:171], v[112:115]
	v_mfma_f32_16x16x32_bf16 v[112:115], v[140:143], v[172:175], v[112:115]
	s_waitcnt lgkmcnt(2)
	v_mfma_f32_16x16x32_bf16 v[108:111], v[128:131], v[176:179], v[108:111]
	v_mfma_f32_16x16x32_bf16 v[108:111], v[132:135], v[180:183], v[108:111]
	v_mfma_f32_16x16x32_bf16 v[104:107], v[136:139], v[176:179], v[104:107]
	v_mfma_f32_16x16x32_bf16 v[104:107], v[140:143], v[180:183], v[104:107]
	s_waitcnt lgkmcnt(0)
	v_mfma_f32_16x16x32_bf16 v[100:103], v[128:131], v[184:187], v[100:103]
	v_mfma_f32_16x16x32_bf16 v[100:103], v[132:135], v[188:191], v[100:103]
	v_mfma_f32_16x16x32_bf16 v[96:99], v[136:139], v[184:187], v[96:99]
	v_mfma_f32_16x16x32_bf16 v[96:99], v[140:143], v[188:191], v[96:99]
	s_setprio 0
	s_setprio 1
	v_mfma_f32_16x16x32_bf16 v[92:95], v[144:147], v[160:163], v[92:95]
	v_mfma_f32_16x16x32_bf16 v[92:95], v[148:151], v[164:167], v[92:95]
	v_mfma_f32_16x16x32_bf16 v[88:91], v[152:155], v[160:163], v[88:91]
	v_mfma_f32_16x16x32_bf16 v[88:91], v[156:159], v[164:167], v[88:91]
	v_mfma_f32_16x16x32_bf16 v[84:87], v[144:147], v[168:171], v[84:87]
	v_mfma_f32_16x16x32_bf16 v[84:87], v[148:151], v[172:175], v[84:87]
	v_mfma_f32_16x16x32_bf16 v[80:83], v[152:155], v[168:171], v[80:83]
	v_mfma_f32_16x16x32_bf16 v[80:83], v[156:159], v[172:175], v[80:83]
	v_mfma_f32_16x16x32_bf16 v[76:79], v[144:147], v[176:179], v[76:79]
	v_mfma_f32_16x16x32_bf16 v[76:79], v[148:151], v[180:183], v[76:79]
	v_mfma_f32_16x16x32_bf16 v[72:75], v[152:155], v[176:179], v[72:75]
	v_mfma_f32_16x16x32_bf16 v[72:75], v[156:159], v[180:183], v[72:75]
	v_mfma_f32_16x16x32_bf16 v[68:71], v[144:147], v[184:187], v[68:71]
	v_mfma_f32_16x16x32_bf16 v[68:71], v[148:151], v[188:191], v[68:71]
	v_mfma_f32_16x16x32_bf16 v[64:67], v[152:155], v[184:187], v[64:67]
	v_mfma_f32_16x16x32_bf16 v[64:67], v[156:159], v[188:191], v[64:67]
	s_setprio 0
	s_barrier
	ds_read_b128 v[160:163], v197 offset:16384
	ds_read_b128 v[164:167], v197 offset:17408
	ds_read_b128 v[168:171], v197 offset:18432
	ds_read_b128 v[172:175], v197 offset:19456
	ds_read_b128 v[176:179], v197 offset:20480
	ds_read_b128 v[180:183], v197 offset:21504
	ds_read_b128 v[184:187], v197 offset:22528
	ds_read_b128 v[188:191], v197 offset:23552
	s_mov_b32 m0, s62
	s_add_i32 s91, s90, 0x20000
	buffer_load_dwordx4 v192, s[8:11], s90 offen lds
	s_mov_b32 m0, s63
	s_nop 0
	buffer_load_dwordx4 v192, s[8:11], s91 offen lds
	s_add_i32 s91, s90, 0x2000
	s_mov_b32 m0, s64
	s_nop 0
	buffer_load_dwordx4 v192, s[8:11], s91 offen lds
	s_add_i32 s91, s90, 0x22000
	s_mov_b32 m0, s65
	s_nop 0
	buffer_load_dwordx4 v192, s[8:11], s91 offen lds
	s_mov_b32 m0, s47
	s_add_i32 s91, s66, 0x10000
	buffer_load_dwordx4 v196, s[4:7], s66 offen lds
	s_mov_b32 m0, s68
	s_nop 0
	buffer_load_dwordx4 v196, s[4:7], s91 offen lds
	s_waitcnt vmcnt(8)
	s_waitcnt lgkmcnt(6)
	s_barrier
	s_setprio 1
	s_waitcnt lgkmcnt(6)
	v_mfma_f32_16x16x32_bf16 v[60:63], v[128:131], v[160:163], v[60:63]
	v_mfma_f32_16x16x32_bf16 v[60:63], v[132:135], v[164:167], v[60:63]
	v_mfma_f32_16x16x32_bf16 v[56:59], v[136:139], v[160:163], v[56:59]
	v_mfma_f32_16x16x32_bf16 v[56:59], v[140:143], v[164:167], v[56:59]
	s_waitcnt lgkmcnt(4)
	v_mfma_f32_16x16x32_bf16 v[52:55], v[128:131], v[168:171], v[52:55]
	v_mfma_f32_16x16x32_bf16 v[52:55], v[132:135], v[172:175], v[52:55]
	v_mfma_f32_16x16x32_bf16 v[48:51], v[136:139], v[168:171], v[48:51]
	v_mfma_f32_16x16x32_bf16 v[48:51], v[140:143], v[172:175], v[48:51]
	s_waitcnt lgkmcnt(2)
	v_mfma_f32_16x16x32_bf16 v[44:47], v[128:131], v[176:179], v[44:47]
	v_mfma_f32_16x16x32_bf16 v[44:47], v[132:135], v[180:183], v[44:47]
	v_mfma_f32_16x16x32_bf16 v[40:43], v[136:139], v[176:179], v[40:43]
	v_mfma_f32_16x16x32_bf16 v[40:43], v[140:143], v[180:183], v[40:43]
	s_waitcnt lgkmcnt(0)
	v_mfma_f32_16x16x32_bf16 v[36:39], v[128:131], v[184:187], v[36:39]
	v_mfma_f32_16x16x32_bf16 v[36:39], v[132:135], v[188:191], v[36:39]
	v_mfma_f32_16x16x32_bf16 v[32:35], v[136:139], v[184:187], v[32:35]
	v_mfma_f32_16x16x32_bf16 v[32:35], v[140:143], v[188:191], v[32:35]
	s_setprio 0
	s_setprio 1
	v_mfma_f32_16x16x32_bf16 v[28:31], v[144:147], v[160:163], v[28:31]
	v_mfma_f32_16x16x32_bf16 v[28:31], v[148:151], v[164:167], v[28:31]
	v_mfma_f32_16x16x32_bf16 v[24:27], v[152:155], v[160:163], v[24:27]
	v_mfma_f32_16x16x32_bf16 v[24:27], v[156:159], v[164:167], v[24:27]
	v_mfma_f32_16x16x32_bf16 v[20:23], v[144:147], v[168:171], v[20:23]
	v_mfma_f32_16x16x32_bf16 v[20:23], v[148:151], v[172:175], v[20:23]
	v_mfma_f32_16x16x32_bf16 v[16:19], v[152:155], v[168:171], v[16:19]
	v_mfma_f32_16x16x32_bf16 v[16:19], v[156:159], v[172:175], v[16:19]
	v_mfma_f32_16x16x32_bf16 v[12:15], v[144:147], v[176:179], v[12:15]
	v_mfma_f32_16x16x32_bf16 v[12:15], v[148:151], v[180:183], v[12:15]
	v_mfma_f32_16x16x32_bf16 v[8:11], v[152:155], v[176:179], v[8:11]
	v_mfma_f32_16x16x32_bf16 v[8:11], v[156:159], v[180:183], v[8:11]
	v_mfma_f32_16x16x32_bf16 v[4:7], v[144:147], v[184:187], v[4:7]
	v_mfma_f32_16x16x32_bf16 v[4:7], v[148:151], v[188:191], v[4:7]
	v_mfma_f32_16x16x32_bf16 v[0:3], v[152:155], v[184:187], v[0:3]
	v_mfma_f32_16x16x32_bf16 v[0:3], v[156:159], v[188:191], v[0:3]
	s_setprio 0
	s_barrier
	ds_read_b128 v[140:143], v203
	ds_read_b128 v[144:147], v204
	ds_read_b128 v[148:151], v205
	ds_read_b128 v[152:155], v206
	ds_read_b128 v[156:159], v207
	ds_read_b128 v[136:139], v208
	ds_read_b128 v[132:135], v209
	ds_read_b128 v[128:131], v210
	ds_read_b128 v[160:163], v197 offset:32768
	ds_read_b128 v[164:167], v197 offset:33792
	ds_read_b128 v[168:171], v197 offset:34816
	ds_read_b128 v[172:175], v197 offset:35840
	ds_read_b128 v[176:179], v197 offset:36864
	ds_read_b128 v[180:183], v197 offset:37888
	ds_read_b128 v[184:187], v197 offset:38912
	ds_read_b128 v[188:191], v197 offset:39936
	s_mov_b32 m0, s69
	s_add_i32 s91, s66, 0x20000
	buffer_load_dwordx4 v196, s[4:7], s91 offen lds
	s_add_i32 s91, s66, 0x30000
	s_mov_b32 m0, s70
	s_nop 0
	buffer_load_dwordx4 v196, s[4:7], s91 offen lds
	s_waitcnt vmcnt(8)
	s_waitcnt lgkmcnt(8)
	s_barrier
	s_setprio 1
	s_waitcnt lgkmcnt(6)
	v_mfma_f32_16x16x32_bf16 v[124:127], v[140:143], v[160:163], v[124:127]
	v_mfma_f32_16x16x32_bf16 v[124:127], v[144:147], v[164:167], v[124:127]
	v_mfma_f32_16x16x32_bf16 v[120:123], v[148:151], v[160:163], v[120:123]
	v_mfma_f32_16x16x32_bf16 v[120:123], v[152:155], v[164:167], v[120:123]
	s_waitcnt lgkmcnt(4)
	v_mfma_f32_16x16x32_bf16 v[116:119], v[140:143], v[168:171], v[116:119]
	v_mfma_f32_16x16x32_bf16 v[116:119], v[144:147], v[172:175], v[116:119]
	v_mfma_f32_16x16x32_bf16 v[112:115], v[148:151], v[168:171], v[112:115]
	v_mfma_f32_16x16x32_bf16 v[112:115], v[152:155], v[172:175], v[112:115]
	s_waitcnt lgkmcnt(2)
	v_mfma_f32_16x16x32_bf16 v[108:111], v[140:143], v[176:179], v[108:111]
	v_mfma_f32_16x16x32_bf16 v[108:111], v[144:147], v[180:183], v[108:111]
	v_mfma_f32_16x16x32_bf16 v[104:107], v[148:151], v[176:179], v[104:107]
	v_mfma_f32_16x16x32_bf16 v[104:107], v[152:155], v[180:183], v[104:107]
	s_waitcnt lgkmcnt(0)
	v_mfma_f32_16x16x32_bf16 v[100:103], v[140:143], v[184:187], v[100:103]
	v_mfma_f32_16x16x32_bf16 v[100:103], v[144:147], v[188:191], v[100:103]
	v_mfma_f32_16x16x32_bf16 v[96:99], v[148:151], v[184:187], v[96:99]
	v_mfma_f32_16x16x32_bf16 v[96:99], v[152:155], v[188:191], v[96:99]
	s_setprio 0
	s_setprio 1
	v_mfma_f32_16x16x32_bf16 v[92:95], v[156:159], v[160:163], v[92:95]
	v_mfma_f32_16x16x32_bf16 v[92:95], v[136:139], v[164:167], v[92:95]
	v_mfma_f32_16x16x32_bf16 v[88:91], v[132:135], v[160:163], v[88:91]
	v_mfma_f32_16x16x32_bf16 v[88:91], v[128:131], v[164:167], v[88:91]
	v_mfma_f32_16x16x32_bf16 v[84:87], v[156:159], v[168:171], v[84:87]
	v_mfma_f32_16x16x32_bf16 v[84:87], v[136:139], v[172:175], v[84:87]
	v_mfma_f32_16x16x32_bf16 v[80:83], v[132:135], v[168:171], v[80:83]
	v_mfma_f32_16x16x32_bf16 v[80:83], v[128:131], v[172:175], v[80:83]
	v_mfma_f32_16x16x32_bf16 v[76:79], v[156:159], v[176:179], v[76:79]
	v_mfma_f32_16x16x32_bf16 v[76:79], v[136:139], v[180:183], v[76:79]
	v_mfma_f32_16x16x32_bf16 v[72:75], v[132:135], v[176:179], v[72:75]
	v_mfma_f32_16x16x32_bf16 v[72:75], v[128:131], v[180:183], v[72:75]
	v_mfma_f32_16x16x32_bf16 v[68:71], v[156:159], v[184:187], v[68:71]
	v_mfma_f32_16x16x32_bf16 v[68:71], v[136:139], v[188:191], v[68:71]
	v_mfma_f32_16x16x32_bf16 v[64:67], v[132:135], v[184:187], v[64:67]
	v_mfma_f32_16x16x32_bf16 v[64:67], v[128:131], v[188:191], v[64:67]
	s_setprio 0
	s_barrier
	ds_read_b128 v[160:163], v197 offset:49152
	ds_read_b128 v[164:167], v197 offset:50176
	ds_read_b128 v[168:171], v197 offset:51200
	ds_read_b128 v[172:175], v197 offset:52224
	ds_read_b128 v[176:179], v197 offset:53248
	ds_read_b128 v[180:183], v197 offset:54272
	ds_read_b128 v[184:187], v197 offset:55296
	ds_read_b128 v[188:191], v197 offset:56320
	s_mov_b32 m0, s72
	s_add_i32 s91, s90, 0x80
	buffer_load_dwordx4 v192, s[8:11], s91 offen lds
	s_add_i32 s91, s90, 0x20080
	s_mov_b32 m0, s73
	s_add_i32 s66, s66, 0x10080
	buffer_load_dwordx4 v192, s[8:11], s91 offen lds
	s_add_i32 s91, s90, 0x2080
	s_mov_b32 m0, s76
	s_add_i32 s90, s90, 0x22080
	buffer_load_dwordx4 v192, s[8:11], s91 offen lds
	s_mov_b32 m0, s77
	s_nop 0
	buffer_load_dwordx4 v192, s[8:11], s90 offen lds
	s_mov_b32 m0, s74
	s_nop 0
	buffer_load_dwordx4 v196, s[4:7], s67 offen lds
	s_mov_b32 m0, s75
	s_nop 0
	buffer_load_dwordx4 v196, s[4:7], s66 offen lds
	s_waitcnt vmcnt(8)
	s_waitcnt lgkmcnt(6)
	s_barrier
	s_setprio 1
	s_waitcnt lgkmcnt(6)
	v_mfma_f32_16x16x32_bf16 v[60:63], v[140:143], v[160:163], v[60:63]
	v_mfma_f32_16x16x32_bf16 v[60:63], v[144:147], v[164:167], v[60:63]
	v_mfma_f32_16x16x32_bf16 v[56:59], v[148:151], v[160:163], v[56:59]
	v_mfma_f32_16x16x32_bf16 v[56:59], v[152:155], v[164:167], v[56:59]
	s_waitcnt lgkmcnt(4)
	v_mfma_f32_16x16x32_bf16 v[52:55], v[140:143], v[168:171], v[52:55]
	v_mfma_f32_16x16x32_bf16 v[52:55], v[144:147], v[172:175], v[52:55]
	v_mfma_f32_16x16x32_bf16 v[48:51], v[148:151], v[168:171], v[48:51]
	v_mfma_f32_16x16x32_bf16 v[48:51], v[152:155], v[172:175], v[48:51]
	s_waitcnt lgkmcnt(2)
	v_mfma_f32_16x16x32_bf16 v[44:47], v[140:143], v[176:179], v[44:47]
	v_mfma_f32_16x16x32_bf16 v[44:47], v[144:147], v[180:183], v[44:47]
	v_mfma_f32_16x16x32_bf16 v[40:43], v[148:151], v[176:179], v[40:43]
	v_mfma_f32_16x16x32_bf16 v[40:43], v[152:155], v[180:183], v[40:43]
	s_waitcnt lgkmcnt(0)
	v_mfma_f32_16x16x32_bf16 v[36:39], v[140:143], v[184:187], v[36:39]
	v_mfma_f32_16x16x32_bf16 v[36:39], v[144:147], v[188:191], v[36:39]
	v_mfma_f32_16x16x32_bf16 v[32:35], v[148:151], v[184:187], v[32:35]
	v_mfma_f32_16x16x32_bf16 v[32:35], v[152:155], v[188:191], v[32:35]
	s_setprio 0
	s_setprio 1
	v_mfma_f32_16x16x32_bf16 v[28:31], v[156:159], v[160:163], v[28:31]
	v_mfma_f32_16x16x32_bf16 v[28:31], v[136:139], v[164:167], v[28:31]
	v_mfma_f32_16x16x32_bf16 v[24:27], v[132:135], v[160:163], v[24:27]
	v_mfma_f32_16x16x32_bf16 v[24:27], v[128:131], v[164:167], v[24:27]
	v_mfma_f32_16x16x32_bf16 v[20:23], v[156:159], v[168:171], v[20:23]
	v_mfma_f32_16x16x32_bf16 v[20:23], v[136:139], v[172:175], v[20:23]
	v_mfma_f32_16x16x32_bf16 v[16:19], v[132:135], v[168:171], v[16:19]
	v_mfma_f32_16x16x32_bf16 v[16:19], v[128:131], v[172:175], v[16:19]
	v_mfma_f32_16x16x32_bf16 v[12:15], v[156:159], v[176:179], v[12:15]
	v_mfma_f32_16x16x32_bf16 v[12:15], v[136:139], v[180:183], v[12:15]
	v_mfma_f32_16x16x32_bf16 v[8:11], v[132:135], v[176:179], v[8:11]
	v_mfma_f32_16x16x32_bf16 v[8:11], v[128:131], v[180:183], v[8:11]
	v_mfma_f32_16x16x32_bf16 v[4:7], v[156:159], v[184:187], v[4:7]
	v_mfma_f32_16x16x32_bf16 v[4:7], v[136:139], v[188:191], v[4:7]
	v_mfma_f32_16x16x32_bf16 v[0:3], v[132:135], v[184:187], v[0:3]
	v_mfma_f32_16x16x32_bf16 v[0:3], v[128:131], v[188:191], v[0:3]
	s_setprio 0
	s_barrier
	s_add_i32 s43, s43, 2
	s_addk_i32 s33, 0x100
	s_addk_i32 s42, 0x100
	s_cmp_gt_u32 s43, 5
	s_cbranch_scc0 .LBB0_254
	s_and_b64 vcc, exec, s[14:15]
	s_cbranch_vccz .LBB0_257
	s_barrier

.LBB0_341:
	s_waitcnt lgkmcnt(0)
	s_add_i32 s16, s60, 0x100
	s_add_i32 s17, s36, 0x100
	s_barrier
	s_setprio 1
	s_waitcnt lgkmcnt(6)
	v_mfma_f32_16x16x32_bf16 v[124:127], v[164:167], v[196:199], 0
	v_mfma_f32_16x16x32_bf16 v[124:127], v[160:163], v[192:195], v[124:127]
	v_mfma_f32_16x16x32_bf16 v[120:123], v[156:159], v[196:199], 0
	v_mfma_f32_16x16x32_bf16 v[120:123], v[152:155], v[192:195], v[120:123]
	s_waitcnt lgkmcnt(4)
	v_mfma_f32_16x16x32_bf16 v[116:119], v[164:167], v[188:191], 0
	v_mfma_f32_16x16x32_bf16 v[116:119], v[160:163], v[184:187], v[116:119]
	v_mfma_f32_16x16x32_bf16 v[112:115], v[156:159], v[188:191], 0
	v_mfma_f32_16x16x32_bf16 v[112:115], v[152:155], v[184:187], v[112:115]
	s_waitcnt lgkmcnt(2)
	v_mfma_f32_16x16x32_bf16 v[108:111], v[164:167], v[180:183], 0
	v_mfma_f32_16x16x32_bf16 v[108:111], v[160:163], v[176:179], v[108:111]
	v_mfma_f32_16x16x32_bf16 v[104:107], v[156:159], v[180:183], 0
	v_mfma_f32_16x16x32_bf16 v[104:107], v[152:155], v[176:179], v[104:107]
	s_waitcnt lgkmcnt(0)
	v_mfma_f32_16x16x32_bf16 v[100:103], v[164:167], v[172:175], 0
	v_mfma_f32_16x16x32_bf16 v[100:103], v[160:163], v[168:171], v[100:103]
	v_mfma_f32_16x16x32_bf16 v[96:99], v[156:159], v[172:175], 0
	v_mfma_f32_16x16x32_bf16 v[96:99], v[152:155], v[168:171], v[96:99]
	s_setprio 0
	s_setprio 1
	v_mfma_f32_16x16x32_bf16 v[92:95], v[148:151], v[196:199], 0
	v_mfma_f32_16x16x32_bf16 v[92:95], v[144:147], v[192:195], v[92:95]
	v_mfma_f32_16x16x32_bf16 v[88:91], v[140:143], v[196:199], 0
	v_mfma_f32_16x16x32_bf16 v[88:91], v[136:139], v[192:195], v[88:91]
	v_mfma_f32_16x16x32_bf16 v[84:87], v[148:151], v[188:191], 0
	v_mfma_f32_16x16x32_bf16 v[84:87], v[144:147], v[184:187], v[84:87]
	v_mfma_f32_16x16x32_bf16 v[80:83], v[140:143], v[188:191], 0
	v_mfma_f32_16x16x32_bf16 v[80:83], v[136:139], v[184:187], v[80:83]
	v_mfma_f32_16x16x32_bf16 v[76:79], v[148:151], v[180:183], 0
	v_mfma_f32_16x16x32_bf16 v[76:79], v[144:147], v[176:179], v[76:79]
	v_mfma_f32_16x16x32_bf16 v[72:75], v[140:143], v[180:183], 0
	v_mfma_f32_16x16x32_bf16 v[72:75], v[136:139], v[176:179], v[72:75]
	v_mfma_f32_16x16x32_bf16 v[68:71], v[148:151], v[172:175], 0
	v_mfma_f32_16x16x32_bf16 v[68:71], v[144:147], v[168:171], v[68:71]
	v_mfma_f32_16x16x32_bf16 v[64:67], v[140:143], v[172:175], 0
	v_mfma_f32_16x16x32_bf16 v[64:67], v[136:139], v[168:171], v[64:67]
	s_setprio 0
	s_barrier
	s_mov_b32 m0, s65
	s_mov_b32 s14, s10
	s_mov_b32 s15, s11
	buffer_load_dwordx4 v215, s[12:15], s17 offen lds
	s_add_i32 s17, s36, 0x100100
	s_mov_b32 m0, s68
	s_and_b64 vcc, exec, s[4:5]
	buffer_load_dwordx4 v215, s[12:15], s17 offen lds
	s_add_i32 s17, s36, 0x10100
	s_mov_b32 m0, s69
	s_nop 0
	buffer_load_dwordx4 v215, s[12:15], s17 offen lds
	s_add_i32 s17, s36, 0x110100
	s_mov_b32 m0, s70
	s_nop 0
	buffer_load_dwordx4 v215, s[12:15], s17 offen lds
	s_mov_b32 m0, s64
	s_add_i32 s14, s60, 0x80100
	buffer_load_dwordx4 v214, s[8:11], s16 offen lds
	s_mov_b32 m0, s71
	s_nop 0
	buffer_load_dwordx4 v214, s[8:11], s14 offen lds
	ds_read_b128 v[196:199], v233 offset:16384
	ds_read_b128 v[192:195], v233 offset:17408
	ds_read_b128 v[188:191], v233 offset:18432
	ds_read_b128 v[184:187], v233 offset:19456
	ds_read_b128 v[180:183], v233 offset:20480
	ds_read_b128 v[176:179], v233 offset:21504
	ds_read_b128 v[172:175], v233 offset:22528
	ds_read_b128 v[168:171], v233 offset:23552
	s_cbranch_vccz .LBB0_359
	s_waitcnt vmcnt(34)
	s_cbranch_execnz .LBB0_344

.LBB0_344:
	s_waitcnt lgkmcnt(0)
	s_add_i32 s4, s60, 0x180
	s_add_i32 s5, s36, 0x180
	s_barrier
	s_setprio 1
	s_waitcnt lgkmcnt(6)
	v_mfma_f32_16x16x32_bf16 v[60:63], v[164:167], v[196:199], 0
	v_mfma_f32_16x16x32_bf16 v[60:63], v[160:163], v[192:195], v[60:63]
	v_mfma_f32_16x16x32_bf16 v[56:59], v[156:159], v[196:199], 0
	v_mfma_f32_16x16x32_bf16 v[56:59], v[152:155], v[192:195], v[56:59]
	s_waitcnt lgkmcnt(4)
	v_mfma_f32_16x16x32_bf16 v[52:55], v[164:167], v[188:191], 0
	v_mfma_f32_16x16x32_bf16 v[52:55], v[160:163], v[184:187], v[52:55]
	v_mfma_f32_16x16x32_bf16 v[48:51], v[156:159], v[188:191], 0
	v_mfma_f32_16x16x32_bf16 v[48:51], v[152:155], v[184:187], v[48:51]
	s_waitcnt lgkmcnt(2)
	v_mfma_f32_16x16x32_bf16 v[44:47], v[164:167], v[180:183], 0
	v_mfma_f32_16x16x32_bf16 v[44:47], v[160:163], v[176:179], v[44:47]
	v_mfma_f32_16x16x32_bf16 v[40:43], v[156:159], v[180:183], 0
	v_mfma_f32_16x16x32_bf16 v[40:43], v[152:155], v[176:179], v[40:43]
	s_waitcnt lgkmcnt(0)
	v_mfma_f32_16x16x32_bf16 v[36:39], v[164:167], v[172:175], 0
	v_mfma_f32_16x16x32_bf16 v[36:39], v[160:163], v[168:171], v[36:39]
	v_mfma_f32_16x16x32_bf16 v[32:35], v[156:159], v[172:175], 0
	v_mfma_f32_16x16x32_bf16 v[32:35], v[152:155], v[168:171], v[32:35]
	s_setprio 0
	s_setprio 1
	v_mfma_f32_16x16x32_bf16 v[28:31], v[148:151], v[196:199], 0
	v_mfma_f32_16x16x32_bf16 v[28:31], v[144:147], v[192:195], v[28:31]
	v_mfma_f32_16x16x32_bf16 v[24:27], v[140:143], v[196:199], 0
	v_mfma_f32_16x16x32_bf16 v[24:27], v[136:139], v[192:195], v[24:27]
	v_mfma_f32_16x16x32_bf16 v[20:23], v[148:151], v[188:191], 0
	v_mfma_f32_16x16x32_bf16 v[20:23], v[144:147], v[184:187], v[20:23]
	v_mfma_f32_16x16x32_bf16 v[16:19], v[140:143], v[188:191], 0
	v_mfma_f32_16x16x32_bf16 v[16:19], v[136:139], v[184:187], v[16:19]
	v_mfma_f32_16x16x32_bf16 v[12:15], v[148:151], v[180:183], 0
	v_mfma_f32_16x16x32_bf16 v[12:15], v[144:147], v[176:179], v[12:15]
	v_mfma_f32_16x16x32_bf16 v[8:11], v[140:143], v[180:183], 0
	v_mfma_f32_16x16x32_bf16 v[8:11], v[136:139], v[176:179], v[8:11]
	v_mfma_f32_16x16x32_bf16 v[4:7], v[148:151], v[172:175], 0
	v_mfma_f32_16x16x32_bf16 v[4:7], v[144:147], v[168:171], v[4:7]
	v_mfma_f32_16x16x32_bf16 v[0:3], v[140:143], v[172:175], 0
	v_mfma_f32_16x16x32_bf16 v[0:3], v[136:139], v[168:171], v[0:3]
	s_setprio 0
	s_barrier
	ds_read_b128 v[164:167], v225
	ds_read_b128 v[160:163], v226
	ds_read_b128 v[156:159], v227
	ds_read_b128 v[152:155], v228
	ds_read_b128 v[148:151], v229
	ds_read_b128 v[144:147], v230
	ds_read_b128 v[140:143], v231
	ds_read_b128 v[136:139], v232
	ds_read_b128 v[168:171], v233 offset:32768
	ds_read_b128 v[172:175], v233 offset:33792
	ds_read_b128 v[176:179], v233 offset:34816
	ds_read_b128 v[180:183], v233 offset:35840
	ds_read_b128 v[184:187], v233 offset:36864
	ds_read_b128 v[188:191], v233 offset:37888
	ds_read_b128 v[192:195], v233 offset:38912
	ds_read_b128 v[196:199], v233 offset:39936
	s_mov_b32 m0, s72
	s_add_i32 s14, s60, 0x100100
	buffer_load_dwordx4 v214, s[8:11], s14 offen lds
	s_add_i32 s14, s60, 0x180100
	s_mov_b32 m0, s73
	s_nop 0
	buffer_load_dwordx4 v214, s[8:11], s14 offen lds
	s_waitcnt vmcnt(10)
	s_waitcnt lgkmcnt(8)
	s_barrier
	s_setprio 1
	s_waitcnt lgkmcnt(6)
	v_mfma_f32_16x16x32_bf16 v[124:127], v[164:167], v[168:171], v[124:127]
	v_mfma_f32_16x16x32_bf16 v[124:127], v[160:163], v[172:175], v[124:127]
	v_mfma_f32_16x16x32_bf16 v[120:123], v[156:159], v[168:171], v[120:123]
	v_mfma_f32_16x16x32_bf16 v[120:123], v[152:155], v[172:175], v[120:123]
	s_waitcnt lgkmcnt(4)
	v_mfma_f32_16x16x32_bf16 v[116:119], v[164:167], v[176:179], v[116:119]
	v_mfma_f32_16x16x32_bf16 v[116:119], v[160:163], v[180:183], v[116:119]
	v_mfma_f32_16x16x32_bf16 v[112:115], v[156:159], v[176:179], v[112:115]
	v_mfma_f32_16x16x32_bf16 v[112:115], v[152:155], v[180:183], v[112:115]
	s_waitcnt lgkmcnt(2)
	v_mfma_f32_16x16x32_bf16 v[108:111], v[164:167], v[184:187], v[108:111]
	v_mfma_f32_16x16x32_bf16 v[108:111], v[160:163], v[188:191], v[108:111]
	v_mfma_f32_16x16x32_bf16 v[104:107], v[156:159], v[184:187], v[104:107]
	v_mfma_f32_16x16x32_bf16 v[104:107], v[152:155], v[188:191], v[104:107]
	s_waitcnt lgkmcnt(0)
	v_mfma_f32_16x16x32_bf16 v[100:103], v[164:167], v[192:195], v[100:103]
	v_mfma_f32_16x16x32_bf16 v[100:103], v[160:163], v[196:199], v[100:103]
	v_mfma_f32_16x16x32_bf16 v[96:99], v[156:159], v[192:195], v[96:99]
	v_mfma_f32_16x16x32_bf16 v[96:99], v[152:155], v[196:199], v[96:99]
	s_setprio 0
	s_setprio 1
	v_mfma_f32_16x16x32_bf16 v[92:95], v[148:151], v[168:171], v[92:95]
	v_mfma_f32_16x16x32_bf16 v[92:95], v[144:147], v[172:175], v[92:95]
	v_mfma_f32_16x16x32_bf16 v[88:91], v[140:143], v[168:171], v[88:91]
	v_mfma_f32_16x16x32_bf16 v[88:91], v[136:139], v[172:175], v[88:91]
	v_mfma_f32_16x16x32_bf16 v[84:87], v[148:151], v[176:179], v[84:87]
	v_mfma_f32_16x16x32_bf16 v[84:87], v[144:147], v[180:183], v[84:87]
	v_mfma_f32_16x16x32_bf16 v[80:83], v[140:143], v[176:179], v[80:83]
	v_mfma_f32_16x16x32_bf16 v[80:83], v[136:139], v[180:183], v[80:83]
	v_mfma_f32_16x16x32_bf16 v[76:79], v[148:151], v[184:187], v[76:79]
	v_mfma_f32_16x16x32_bf16 v[76:79], v[144:147], v[188:191], v[76:79]
	v_mfma_f32_16x16x32_bf16 v[72:75], v[140:143], v[184:187], v[72:75]
	v_mfma_f32_16x16x32_bf16 v[72:75], v[136:139], v[188:191], v[72:75]
	v_mfma_f32_16x16x32_bf16 v[68:71], v[148:151], v[192:195], v[68:71]
	v_mfma_f32_16x16x32_bf16 v[68:71], v[144:147], v[196:199], v[68:71]
	v_mfma_f32_16x16x32_bf16 v[64:67], v[140:143], v[192:195], v[64:67]
	v_mfma_f32_16x16x32_bf16 v[64:67], v[136:139], v[196:199], v[64:67]
	s_setprio 0
	s_barrier
	ds_read_b128 v[168:171], v233 offset:49152
	ds_read_b128 v[172:175], v233 offset:50176
	ds_read_b128 v[176:179], v233 offset:51200
	ds_read_b128 v[180:183], v233 offset:52224
	ds_read_b128 v[184:187], v233 offset:53248
	ds_read_b128 v[188:191], v233 offset:54272
	ds_read_b128 v[192:195], v233 offset:55296
	ds_read_b128 v[196:199], v233 offset:56320
	s_mov_b32 m0, s76
	s_mov_b32 s14, s10
	s_mov_b32 s15, s11
	buffer_load_dwordx4 v215, s[12:15], s5 offen lds
	s_add_i32 s5, s36, 0x100180
	s_mov_b32 m0, s77
	s_nop 0
	buffer_load_dwordx4 v215, s[12:15], s5 offen lds
	s_add_i32 s5, s36, 0x10180
	s_mov_b32 m0, s80
	s_nop 0
	buffer_load_dwordx4 v215, s[12:15], s5 offen lds
	s_add_i32 s5, s36, 0x110180
	s_mov_b32 m0, s81
	s_nop 0
	buffer_load_dwordx4 v215, s[12:15], s5 offen lds
	s_mov_b32 m0, s78
	s_nop 0
	buffer_load_dwordx4 v214, s[8:11], s4 offen lds
	s_add_i32 s4, s60, 0x80180
	s_mov_b32 m0, s79
	s_nop 0
	buffer_load_dwordx4 v214, s[8:11], s4 offen lds
	s_waitcnt vmcnt(8)
	s_waitcnt lgkmcnt(6)
	s_barrier
	s_setprio 1
	s_waitcnt lgkmcnt(6)
	v_mfma_f32_16x16x32_bf16 v[60:63], v[164:167], v[168:171], v[60:63]
	v_mfma_f32_16x16x32_bf16 v[60:63], v[160:163], v[172:175], v[60:63]
	v_mfma_f32_16x16x32_bf16 v[56:59], v[156:159], v[168:171], v[56:59]
	v_mfma_f32_16x16x32_bf16 v[56:59], v[152:155], v[172:175], v[56:59]
	s_waitcnt lgkmcnt(4)
	v_mfma_f32_16x16x32_bf16 v[52:55], v[164:167], v[176:179], v[52:55]
	v_mfma_f32_16x16x32_bf16 v[52:55], v[160:163], v[180:183], v[52:55]
	v_mfma_f32_16x16x32_bf16 v[48:51], v[156:159], v[176:179], v[48:51]
	v_mfma_f32_16x16x32_bf16 v[48:51], v[152:155], v[180:183], v[48:51]
	s_waitcnt lgkmcnt(2)
	v_mfma_f32_16x16x32_bf16 v[44:47], v[164:167], v[184:187], v[44:47]
	v_mfma_f32_16x16x32_bf16 v[44:47], v[160:163], v[188:191], v[44:47]
	v_mfma_f32_16x16x32_bf16 v[40:43], v[156:159], v[184:187], v[40:43]
	v_mfma_f32_16x16x32_bf16 v[40:43], v[152:155], v[188:191], v[40:43]
	s_waitcnt lgkmcnt(0)
	v_mfma_f32_16x16x32_bf16 v[36:39], v[164:167], v[192:195], v[36:39]
	v_mfma_f32_16x16x32_bf16 v[36:39], v[160:163], v[196:199], v[36:39]
	v_mfma_f32_16x16x32_bf16 v[32:35], v[156:159], v[192:195], v[32:35]
	v_mfma_f32_16x16x32_bf16 v[32:35], v[152:155], v[196:199], v[32:35]
	s_setprio 0
	s_setprio 1
	v_mfma_f32_16x16x32_bf16 v[28:31], v[148:151], v[168:171], v[28:31]
	v_mfma_f32_16x16x32_bf16 v[28:31], v[144:147], v[172:175], v[28:31]
	v_mfma_f32_16x16x32_bf16 v[24:27], v[140:143], v[168:171], v[24:27]
	v_mfma_f32_16x16x32_bf16 v[24:27], v[136:139], v[172:175], v[24:27]
	v_mfma_f32_16x16x32_bf16 v[20:23], v[148:151], v[176:179], v[20:23]
	v_mfma_f32_16x16x32_bf16 v[20:23], v[144:147], v[180:183], v[20:23]
	v_mfma_f32_16x16x32_bf16 v[16:19], v[140:143], v[176:179], v[16:19]
	v_mfma_f32_16x16x32_bf16 v[16:19], v[136:139], v[180:183], v[16:19]
	v_mfma_f32_16x16x32_bf16 v[12:15], v[148:151], v[184:187], v[12:15]
	v_mfma_f32_16x16x32_bf16 v[12:15], v[144:147], v[188:191], v[12:15]
	v_mfma_f32_16x16x32_bf16 v[8:11], v[140:143], v[184:187], v[8:11]
	v_mfma_f32_16x16x32_bf16 v[8:11], v[136:139], v[188:191], v[8:11]
	v_mfma_f32_16x16x32_bf16 v[4:7], v[148:151], v[192:195], v[4:7]
	v_mfma_f32_16x16x32_bf16 v[4:7], v[144:147], v[196:199], v[4:7]
	v_mfma_f32_16x16x32_bf16 v[0:3], v[140:143], v[192:195], v[0:3]
	v_mfma_f32_16x16x32_bf16 v[0:3], v[136:139], v[196:199], v[0:3]
	s_setprio 0
	s_barrier
	s_waitcnt vmcnt(14)
	v_mul_f32_e32 v132, 0x42800000, v132
	v_mul_f32_e32 v128, 0x42800000, v128
	v_mul_f32_e32 v133, 0x42800000, v133
	v_mul_f32_e32 v129, 0x42800000, v129
	v_mul_f32_e32 v134, 0x42800000, v134
	v_mul_f32_e32 v130, 0x42800000, v130
	v_mul_f32_e32 v135, 0x42800000, v135
	v_mul_f32_e32 v131, 0x42800000, v131
	v_cvt_pk_fp8_f32 v204, v128, v132
	v_cvt_pk_fp8_f32 v234, v129, v133
	v_cvt_pk_fp8_f32 v235, v130, v134
	v_cvt_pk_fp8_f32 v236, v131, v135
	s_add_i32 s33, s36, 0x200
	s_mov_b32 s61, 0
	s_mov_b32 s66, s75
	s_mov_b32 s94, s86
	s_branch .LBB0_347

.LBB0_347:
	v_mov_b32_e32 v152, v204
	v_mov_b32_e32 v153, v234
	v_mov_b32_e32 v154, v235
	v_mov_b32_e32 v155, v236
	ds_read_b128 v[158:161], v217
	ds_read_b128 v[162:165], v218
	ds_read_b128 v[166:169], v219
	ds_read_b128 v[170:173], v220
	ds_read_b128 v[148:151], v221
	ds_read_b128 v[144:147], v222
	ds_read_b128 v[140:143], v223
	ds_read_b128 v[136:139], v224
	ds_read_b128 v[174:177], v233
	ds_read_b128 v[178:181], v233 offset:1024
	ds_read_b128 v[182:185], v233 offset:2048
	ds_read_b128 v[186:189], v233 offset:3072
	ds_read_b128 v[190:193], v233 offset:4096
	ds_read_b128 v[194:197], v233 offset:5120
	ds_read_b128 v[234:237], v233 offset:6144
	ds_read_b128 v[238:241], v233 offset:7168
	s_add_i32 s4, s60, s61
	s_mov_b32 s46, s94
	s_add_i32 s94, s94, 1
	s_add_i32 s5, s4, 0x200
	s_add_i32 s16, s33, s61
	s_cmpk_eq_i32 s61, 0x1e00
	s_cselect_b32 s47, s90, s5
	s_cselect_b32 s97, s91, s16
	s_add_i32 s96, s47, 0x80
	s_mov_b32 m0, s82
	s_add_i32 s5, s4, 0x100180
	buffer_load_dwordx4 v214, s[8:11], s5 offen lds
	s_add_i32 s4, s4, 0x180180
	s_mov_b32 m0, s85
	s_add_i32 vcc_lo, s97, 0x80
	buffer_load_dwordx4 v214, s[8:11], s4 offen lds
	s_lshr_b32 s4, s94, 2
	s_mul_i32 s5, s4, s34
	s_add_i32 s16, s5, s2
	s_cmp_lt_i32 s4, s3
	s_cselect_b64 s[4:5], -1, 0
	s_and_b64 s[44:45], s[4:5], exec
	s_cselect_b32 s16, s16, 0
	s_bfe_u32 s17, s94, 0x10001
	s_or_b32 s17, s17, s83
	s_bfe_u32 s67, s16, 0x50007
	s_bfe_u32 s36, s16, 0x50002
	s_and_b32 s95, s16, 3
	s_cmpk_gt_i32 s16, 0xfff
	s_cselect_b64 s[44:45], -1, 0
	v_lshl_or_b32 v156, s17, 3, v216
	s_and_b64 s[16:17], s[44:45], exec
	s_cselect_b32 s16, s25, s21
	s_cselect_b32 s17, s24, s20
	s_lshl_b32 vcc_hi, s67, 23
	s_add_u32 s17, s17, vcc_hi
	s_addc_u32 s16, s16, 0
	s_lshl_b32 vcc_hi, s36, 18
	s_add_u32 s17, s17, vcc_hi
	s_addc_u32 vcc_hi, s16, 0
	s_lshl_b32 s16, s95, 9
	s_add_u32 s16, s17, s16
	v_and_or_b32 v204, s66, 2, v200
	s_addc_u32 s17, vcc_hi, 0
	v_lshlrev_b64 v[128:129], 11, v[204:205]
	v_lshl_add_u64 v[128:129], s[16:17], 0, v[128:129]
	v_lshlrev_b32_e32 v204, 4, v156
	v_lshl_add_u64 v[132:133], v[128:129], 0, v[204:205]
	global_load_dwordx4 v[128:131], v[132:133], off nt
	s_nop 0
	global_load_dwordx4 v[132:135], v[132:133], off offset:2048 nt
	s_waitcnt vmcnt(10)
	s_waitcnt lgkmcnt(8)
	s_barrier
	s_setprio 1
	s_waitcnt lgkmcnt(6)
	v_mfma_f32_16x16x32_bf16 v[124:127], v[158:161], v[174:177], v[124:127]
	v_mfma_f32_16x16x32_bf16 v[124:127], v[162:165], v[178:181], v[124:127]
	v_mfma_f32_16x16x32_bf16 v[120:123], v[166:169], v[174:177], v[120:123]
	v_mfma_f32_16x16x32_bf16 v[120:123], v[170:173], v[178:181], v[120:123]
	s_waitcnt lgkmcnt(4)
	v_mfma_f32_16x16x32_bf16 v[116:119], v[158:161], v[182:185], v[116:119]
	v_mfma_f32_16x16x32_bf16 v[116:119], v[162:165], v[186:189], v[116:119]
	v_mfma_f32_16x16x32_bf16 v[112:115], v[166:169], v[182:185], v[112:115]
	v_mfma_f32_16x16x32_bf16 v[112:115], v[170:173], v[186:189], v[112:115]
	s_waitcnt lgkmcnt(2)
	v_mfma_f32_16x16x32_bf16 v[108:111], v[158:161], v[190:193], v[108:111]
	v_mfma_f32_16x16x32_bf16 v[108:111], v[162:165], v[194:197], v[108:111]
	v_mfma_f32_16x16x32_bf16 v[104:107], v[166:169], v[190:193], v[104:107]
	v_mfma_f32_16x16x32_bf16 v[104:107], v[170:173], v[194:197], v[104:107]
	s_waitcnt lgkmcnt(0)
	v_mfma_f32_16x16x32_bf16 v[100:103], v[158:161], v[234:237], v[100:103]
	v_mfma_f32_16x16x32_bf16 v[100:103], v[162:165], v[238:241], v[100:103]
	v_mfma_f32_16x16x32_bf16 v[96:99], v[166:169], v[234:237], v[96:99]
	v_mfma_f32_16x16x32_bf16 v[96:99], v[170:173], v[238:241], v[96:99]
	s_setprio 0
	s_setprio 1
	v_mfma_f32_16x16x32_bf16 v[92:95], v[148:151], v[174:177], v[92:95]
	v_mfma_f32_16x16x32_bf16 v[92:95], v[144:147], v[178:181], v[92:95]
	v_mfma_f32_16x16x32_bf16 v[88:91], v[140:143], v[174:177], v[88:91]
	v_mfma_f32_16x16x32_bf16 v[88:91], v[136:139], v[178:181], v[88:91]
	v_mfma_f32_16x16x32_bf16 v[84:87], v[148:151], v[182:185], v[84:87]
	v_mfma_f32_16x16x32_bf16 v[84:87], v[144:147], v[186:189], v[84:87]
	v_mfma_f32_16x16x32_bf16 v[80:83], v[140:143], v[182:185], v[80:83]
	v_mfma_f32_16x16x32_bf16 v[80:83], v[136:139], v[186:189], v[80:83]
	v_mfma_f32_16x16x32_bf16 v[76:79], v[148:151], v[190:193], v[76:79]
	v_mfma_f32_16x16x32_bf16 v[76:79], v[144:147], v[194:197], v[76:79]
	v_mfma_f32_16x16x32_bf16 v[72:75], v[140:143], v[190:193], v[72:75]
	v_mfma_f32_16x16x32_bf16 v[72:75], v[136:139], v[194:197], v[72:75]
	v_mfma_f32_16x16x32_bf16 v[68:71], v[148:151], v[234:237], v[68:71]
	v_mfma_f32_16x16x32_bf16 v[68:71], v[144:147], v[238:241], v[68:71]
	v_mfma_f32_16x16x32_bf16 v[64:67], v[140:143], v[234:237], v[64:67]
	v_mfma_f32_16x16x32_bf16 v[64:67], v[136:139], v[238:241], v[64:67]
	s_setprio 0
	s_barrier
	ds_read_b128 v[174:177], v233 offset:16384
	ds_read_b128 v[178:181], v233 offset:17408
	ds_read_b128 v[182:185], v233 offset:18432
	ds_read_b128 v[186:189], v233 offset:19456
	ds_read_b128 v[190:193], v233 offset:20480
	ds_read_b128 v[194:197], v233 offset:21504
	ds_read_b128 v[234:237], v233 offset:22528
	ds_read_b128 v[238:241], v233 offset:23552
	s_mov_b32 m0, s65
	s_add_i32 s16, s97, 0x100000
	buffer_load_dwordx4 v215, s[12:15], s97 offen lds
	s_mov_b32 m0, s68
	s_nop 0
	buffer_load_dwordx4 v215, s[12:15], s16 offen lds
	s_add_i32 s16, s97, 0x10000
	s_mov_b32 m0, s69
	s_nop 0
	buffer_load_dwordx4 v215, s[12:15], s16 offen lds
	s_add_i32 s16, s97, 0x110000
	s_mov_b32 m0, s70
	s_nop 0
	buffer_load_dwordx4 v215, s[12:15], s16 offen lds
	s_mov_b32 m0, s64
	s_add_i32 s16, s47, 0x80000
	buffer_load_dwordx4 v214, s[8:11], s47 offen lds
	s_mov_b32 m0, s71
	s_nop 0
	buffer_load_dwordx4 v214, s[8:11], s16 offen lds
	s_waitcnt vmcnt(10)
	s_waitcnt lgkmcnt(6)
	s_barrier
	s_setprio 1
	s_waitcnt lgkmcnt(6)
	v_mfma_f32_16x16x32_bf16 v[60:63], v[158:161], v[174:177], v[60:63]
	v_mfma_f32_16x16x32_bf16 v[60:63], v[162:165], v[178:181], v[60:63]
	v_mfma_f32_16x16x32_bf16 v[56:59], v[166:169], v[174:177], v[56:59]
	v_mfma_f32_16x16x32_bf16 v[56:59], v[170:173], v[178:181], v[56:59]
	s_waitcnt lgkmcnt(4)
	v_mfma_f32_16x16x32_bf16 v[52:55], v[158:161], v[182:185], v[52:55]
	v_mfma_f32_16x16x32_bf16 v[52:55], v[162:165], v[186:189], v[52:55]
	v_mfma_f32_16x16x32_bf16 v[48:51], v[166:169], v[182:185], v[48:51]
	v_mfma_f32_16x16x32_bf16 v[48:51], v[170:173], v[186:189], v[48:51]
	s_waitcnt lgkmcnt(2)
	v_mfma_f32_16x16x32_bf16 v[44:47], v[158:161], v[190:193], v[44:47]
	v_mfma_f32_16x16x32_bf16 v[44:47], v[162:165], v[194:197], v[44:47]
	v_mfma_f32_16x16x32_bf16 v[40:43], v[166:169], v[190:193], v[40:43]
	v_mfma_f32_16x16x32_bf16 v[40:43], v[170:173], v[194:197], v[40:43]
	s_waitcnt lgkmcnt(0)
	v_mfma_f32_16x16x32_bf16 v[36:39], v[158:161], v[234:237], v[36:39]
	v_mfma_f32_16x16x32_bf16 v[36:39], v[162:165], v[238:241], v[36:39]
	v_mfma_f32_16x16x32_bf16 v[32:35], v[166:169], v[234:237], v[32:35]
	v_mfma_f32_16x16x32_bf16 v[32:35], v[170:173], v[238:241], v[32:35]
	s_setprio 0
	s_setprio 1
	v_mfma_f32_16x16x32_bf16 v[28:31], v[148:151], v[174:177], v[28:31]
	v_mfma_f32_16x16x32_bf16 v[28:31], v[144:147], v[178:181], v[28:31]
	v_mfma_f32_16x16x32_bf16 v[24:27], v[140:143], v[174:177], v[24:27]
	v_mfma_f32_16x16x32_bf16 v[24:27], v[136:139], v[178:181], v[24:27]
	v_mfma_f32_16x16x32_bf16 v[20:23], v[148:151], v[182:185], v[20:23]
	v_mfma_f32_16x16x32_bf16 v[20:23], v[144:147], v[186:189], v[20:23]
	v_mfma_f32_16x16x32_bf16 v[16:19], v[140:143], v[182:185], v[16:19]
	v_mfma_f32_16x16x32_bf16 v[16:19], v[136:139], v[186:189], v[16:19]
	v_mfma_f32_16x16x32_bf16 v[12:15], v[148:151], v[190:193], v[12:15]
	v_mfma_f32_16x16x32_bf16 v[12:15], v[144:147], v[194:197], v[12:15]
	v_mfma_f32_16x16x32_bf16 v[8:11], v[140:143], v[190:193], v[8:11]
	v_mfma_f32_16x16x32_bf16 v[8:11], v[136:139], v[194:197], v[8:11]
	v_mfma_f32_16x16x32_bf16 v[4:7], v[148:151], v[234:237], v[4:7]
	v_mfma_f32_16x16x32_bf16 v[4:7], v[144:147], v[238:241], v[4:7]
	v_mfma_f32_16x16x32_bf16 v[0:3], v[140:143], v[234:237], v[0:3]
	v_mfma_f32_16x16x32_bf16 v[0:3], v[136:139], v[238:241], v[0:3]
	s_setprio 0
	s_barrier
	ds_read_b128 v[136:139], v225
	ds_read_b128 v[140:143], v226
	ds_read_b128 v[144:147], v227
	ds_read_b128 v[148:151], v228
	ds_read_b128 v[158:161], v229
	ds_read_b128 v[162:165], v230
	ds_read_b128 v[166:169], v231
	ds_read_b128 v[170:173], v232
	ds_read_b128 v[174:177], v233 offset:32768
	ds_read_b128 v[178:181], v233 offset:33792
	ds_read_b128 v[182:185], v233 offset:34816
	ds_read_b128 v[186:189], v233 offset:35840
	ds_read_b128 v[190:193], v233 offset:36864
	ds_read_b128 v[194:197], v233 offset:37888
	ds_read_b128 v[234:237], v233 offset:38912
	ds_read_b128 v[238:241], v233 offset:39936
	s_mov_b32 m0, s72
	s_add_i32 s16, s47, 0x100000
	buffer_load_dwordx4 v214, s[8:11], s16 offen lds
	s_add_i32 s16, s47, 0x180000
	s_mov_b32 m0, s73
	s_nop 0
	buffer_load_dwordx4 v214, s[8:11], s16 offen lds
	s_waitcnt vmcnt(10)
	s_waitcnt lgkmcnt(8)
	s_barrier
	s_setprio 1
	s_waitcnt lgkmcnt(6)
	v_mfma_f32_16x16x32_bf16 v[124:127], v[136:139], v[174:177], v[124:127]
	v_mfma_f32_16x16x32_bf16 v[124:127], v[140:143], v[178:181], v[124:127]
	v_mfma_f32_16x16x32_bf16 v[120:123], v[144:147], v[174:177], v[120:123]
	v_mfma_f32_16x16x32_bf16 v[120:123], v[148:151], v[178:181], v[120:123]
	s_waitcnt lgkmcnt(4)
	v_mfma_f32_16x16x32_bf16 v[116:119], v[136:139], v[182:185], v[116:119]
	v_mfma_f32_16x16x32_bf16 v[116:119], v[140:143], v[186:189], v[116:119]
	v_mfma_f32_16x16x32_bf16 v[112:115], v[144:147], v[182:185], v[112:115]
	v_mfma_f32_16x16x32_bf16 v[112:115], v[148:151], v[186:189], v[112:115]
	s_waitcnt lgkmcnt(2)
	v_mfma_f32_16x16x32_bf16 v[108:111], v[136:139], v[190:193], v[108:111]
	v_mfma_f32_16x16x32_bf16 v[108:111], v[140:143], v[194:197], v[108:111]
	v_mfma_f32_16x16x32_bf16 v[104:107], v[144:147], v[190:193], v[104:107]
	v_mfma_f32_16x16x32_bf16 v[104:107], v[148:151], v[194:197], v[104:107]
	s_waitcnt lgkmcnt(0)
	v_mfma_f32_16x16x32_bf16 v[100:103], v[136:139], v[234:237], v[100:103]
	v_mfma_f32_16x16x32_bf16 v[100:103], v[140:143], v[238:241], v[100:103]
	v_mfma_f32_16x16x32_bf16 v[96:99], v[144:147], v[234:237], v[96:99]
	v_mfma_f32_16x16x32_bf16 v[96:99], v[148:151], v[238:241], v[96:99]
	s_setprio 0
	s_setprio 1
	v_mfma_f32_16x16x32_bf16 v[92:95], v[158:161], v[174:177], v[92:95]
	v_mfma_f32_16x16x32_bf16 v[92:95], v[162:165], v[178:181], v[92:95]
	v_mfma_f32_16x16x32_bf16 v[88:91], v[166:169], v[174:177], v[88:91]
	v_mfma_f32_16x16x32_bf16 v[88:91], v[170:173], v[178:181], v[88:91]
	v_mfma_f32_16x16x32_bf16 v[84:87], v[158:161], v[182:185], v[84:87]
	v_mfma_f32_16x16x32_bf16 v[84:87], v[162:165], v[186:189], v[84:87]
	v_mfma_f32_16x16x32_bf16 v[80:83], v[166:169], v[182:185], v[80:83]
	v_mfma_f32_16x16x32_bf16 v[80:83], v[170:173], v[186:189], v[80:83]
	v_mfma_f32_16x16x32_bf16 v[76:79], v[158:161], v[190:193], v[76:79]
	v_mfma_f32_16x16x32_bf16 v[76:79], v[162:165], v[194:197], v[76:79]
	v_mfma_f32_16x16x32_bf16 v[72:75], v[166:169], v[190:193], v[72:75]
	v_mfma_f32_16x16x32_bf16 v[72:75], v[170:173], v[194:197], v[72:75]
	v_mfma_f32_16x16x32_bf16 v[68:71], v[158:161], v[234:237], v[68:71]
	v_mfma_f32_16x16x32_bf16 v[68:71], v[162:165], v[238:241], v[68:71]
	v_mfma_f32_16x16x32_bf16 v[64:67], v[166:169], v[234:237], v[64:67]
	v_mfma_f32_16x16x32_bf16 v[64:67], v[170:173], v[238:241], v[64:67]
	s_setprio 0
	s_barrier
	ds_read_b128 v[174:177], v233 offset:49152
	ds_read_b128 v[178:181], v233 offset:50176
	ds_read_b128 v[182:185], v233 offset:51200
	ds_read_b128 v[186:189], v233 offset:52224
	ds_read_b128 v[190:193], v233 offset:53248
	ds_read_b128 v[194:197], v233 offset:54272
	ds_read_b128 v[234:237], v233 offset:55296
	ds_read_b128 v[238:241], v233 offset:56320
	s_mov_b32 m0, s76
	s_add_i32 s16, s97, 0x100080
	buffer_load_dwordx4 v215, s[12:15], vcc_lo offen lds
	s_mov_b32 m0, s77
	s_add_i32 s47, s47, 0x80080
	buffer_load_dwordx4 v215, s[12:15], s16 offen lds
	s_add_i32 s16, s97, 0x10080
	s_mov_b32 m0, s80
	s_add_i32 s97, s97, 0x110080
	buffer_load_dwordx4 v215, s[12:15], s16 offen lds
	s_mov_b32 m0, s81
	s_nop 0
	buffer_load_dwordx4 v215, s[12:15], s97 offen lds
	s_mov_b32 m0, s78
	s_nop 0
	buffer_load_dwordx4 v214, s[8:11], s96 offen lds
	s_mov_b32 m0, s79
	s_nop 0
	buffer_load_dwordx4 v214, s[8:11], s47 offen lds
	s_waitcnt vmcnt(8)
	s_waitcnt lgkmcnt(6)
	s_barrier
	s_setprio 1
	s_waitcnt lgkmcnt(6)
	v_mfma_f32_16x16x32_bf16 v[60:63], v[136:139], v[174:177], v[60:63]
	v_mfma_f32_16x16x32_bf16 v[60:63], v[140:143], v[178:181], v[60:63]
	v_mfma_f32_16x16x32_bf16 v[56:59], v[144:147], v[174:177], v[56:59]
	v_mfma_f32_16x16x32_bf16 v[56:59], v[148:151], v[178:181], v[56:59]
	s_waitcnt lgkmcnt(4)
	v_mfma_f32_16x16x32_bf16 v[52:55], v[136:139], v[182:185], v[52:55]
	v_mfma_f32_16x16x32_bf16 v[52:55], v[140:143], v[186:189], v[52:55]
	v_mfma_f32_16x16x32_bf16 v[48:51], v[144:147], v[182:185], v[48:51]
	v_mfma_f32_16x16x32_bf16 v[48:51], v[148:151], v[186:189], v[48:51]
	s_waitcnt lgkmcnt(2)
	v_mfma_f32_16x16x32_bf16 v[44:47], v[136:139], v[190:193], v[44:47]
	v_mfma_f32_16x16x32_bf16 v[44:47], v[140:143], v[194:197], v[44:47]
	v_mfma_f32_16x16x32_bf16 v[40:43], v[144:147], v[190:193], v[40:43]
	v_mfma_f32_16x16x32_bf16 v[40:43], v[148:151], v[194:197], v[40:43]
	s_waitcnt lgkmcnt(0)
	v_mfma_f32_16x16x32_bf16 v[36:39], v[136:139], v[234:237], v[36:39]
	v_mfma_f32_16x16x32_bf16 v[36:39], v[140:143], v[238:241], v[36:39]
	v_mfma_f32_16x16x32_bf16 v[32:35], v[144:147], v[234:237], v[32:35]
	v_mfma_f32_16x16x32_bf16 v[32:35], v[148:151], v[238:241], v[32:35]
	s_setprio 0
	s_setprio 1
	v_mfma_f32_16x16x32_bf16 v[28:31], v[158:161], v[174:177], v[28:31]
	v_mfma_f32_16x16x32_bf16 v[28:31], v[162:165], v[178:181], v[28:31]
	v_mfma_f32_16x16x32_bf16 v[24:27], v[166:169], v[174:177], v[24:27]
	v_mfma_f32_16x16x32_bf16 v[24:27], v[170:173], v[178:181], v[24:27]
	v_mfma_f32_16x16x32_bf16 v[20:23], v[158:161], v[182:185], v[20:23]
	v_mfma_f32_16x16x32_bf16 v[20:23], v[162:165], v[186:189], v[20:23]
	v_mfma_f32_16x16x32_bf16 v[16:19], v[166:169], v[182:185], v[16:19]
	v_mfma_f32_16x16x32_bf16 v[16:19], v[170:173], v[186:189], v[16:19]
	v_mfma_f32_16x16x32_bf16 v[12:15], v[158:161], v[190:193], v[12:15]
	v_mfma_f32_16x16x32_bf16 v[12:15], v[162:165], v[194:197], v[12:15]
	v_mfma_f32_16x16x32_bf16 v[8:11], v[166:169], v[190:193], v[8:11]
	v_mfma_f32_16x16x32_bf16 v[8:11], v[170:173], v[194:197], v[8:11]
	v_mfma_f32_16x16x32_bf16 v[4:7], v[158:161], v[234:237], v[4:7]
	v_mfma_f32_16x16x32_bf16 v[4:7], v[162:165], v[238:241], v[4:7]
	v_mfma_f32_16x16x32_bf16 v[0:3], v[166:169], v[234:237], v[0:3]
	v_mfma_f32_16x16x32_bf16 v[0:3], v[170:173], v[238:241], v[0:3]
	s_setprio 0
	s_barrier
	s_bitcmp0_b32 s46, 0
	s_waitcnt vmcnt(15)
	v_mul_f32_e32 v128, 0x42800000, v128
	s_waitcnt vmcnt(14)
	v_mul_f32_e32 v132, 0x42800000, v132
	v_mul_f32_e32 v129, 0x42800000, v129
	v_mul_f32_e32 v133, 0x42800000, v133
	v_mul_f32_e32 v130, 0x42800000, v130
	v_mul_f32_e32 v134, 0x42800000, v134
	v_mul_f32_e32 v131, 0x42800000, v131
	v_mul_f32_e32 v135, 0x42800000, v135
	s_mov_b64 s[46:47], -1
	s_cbranch_scc0 .LBB0_350
	s_andn2_b64 vcc, exec, s[46:47]
	s_cbranch_vccnz .LBB0_346
	s_branch .LBB0_351

.LBB0_589:
	s_waitcnt lgkmcnt(0)
	s_add_i32 s33, s60, 0x100
	s_add_i32 s43, s42, 0x100
	s_barrier
	s_setprio 1
	s_waitcnt lgkmcnt(6)
	v_mfma_f32_16x16x32_bf16 v[124:127], v[164:167], v[196:199], 0
	v_mfma_f32_16x16x32_bf16 v[124:127], v[160:163], v[192:195], v[124:127]
	v_mfma_f32_16x16x32_bf16 v[120:123], v[156:159], v[196:199], 0
	v_mfma_f32_16x16x32_bf16 v[120:123], v[152:155], v[192:195], v[120:123]
	s_waitcnt lgkmcnt(4)
	v_mfma_f32_16x16x32_bf16 v[116:119], v[164:167], v[188:191], 0
	v_mfma_f32_16x16x32_bf16 v[116:119], v[160:163], v[184:187], v[116:119]
	v_mfma_f32_16x16x32_bf16 v[112:115], v[156:159], v[188:191], 0
	v_mfma_f32_16x16x32_bf16 v[112:115], v[152:155], v[184:187], v[112:115]
	s_waitcnt lgkmcnt(2)
	v_mfma_f32_16x16x32_bf16 v[108:111], v[164:167], v[180:183], 0
	v_mfma_f32_16x16x32_bf16 v[108:111], v[160:163], v[176:179], v[108:111]
	v_mfma_f32_16x16x32_bf16 v[104:107], v[156:159], v[180:183], 0
	v_mfma_f32_16x16x32_bf16 v[104:107], v[152:155], v[176:179], v[104:107]
	s_waitcnt lgkmcnt(0)
	v_mfma_f32_16x16x32_bf16 v[100:103], v[164:167], v[172:175], 0
	v_mfma_f32_16x16x32_bf16 v[100:103], v[160:163], v[168:171], v[100:103]
	v_mfma_f32_16x16x32_bf16 v[96:99], v[156:159], v[172:175], 0
	v_mfma_f32_16x16x32_bf16 v[96:99], v[152:155], v[168:171], v[96:99]
	s_setprio 0
	s_setprio 1
	v_mfma_f32_16x16x32_bf16 v[92:95], v[148:151], v[196:199], 0
	v_mfma_f32_16x16x32_bf16 v[92:95], v[144:147], v[192:195], v[92:95]
	v_mfma_f32_16x16x32_bf16 v[88:91], v[140:143], v[196:199], 0
	v_mfma_f32_16x16x32_bf16 v[88:91], v[136:139], v[192:195], v[88:91]
	v_mfma_f32_16x16x32_bf16 v[84:87], v[148:151], v[188:191], 0
	v_mfma_f32_16x16x32_bf16 v[84:87], v[144:147], v[184:187], v[84:87]
	v_mfma_f32_16x16x32_bf16 v[80:83], v[140:143], v[188:191], 0
	v_mfma_f32_16x16x32_bf16 v[80:83], v[136:139], v[184:187], v[80:83]
	v_mfma_f32_16x16x32_bf16 v[76:79], v[148:151], v[180:183], 0
	v_mfma_f32_16x16x32_bf16 v[76:79], v[144:147], v[176:179], v[76:79]
	v_mfma_f32_16x16x32_bf16 v[72:75], v[140:143], v[180:183], 0
	v_mfma_f32_16x16x32_bf16 v[72:75], v[136:139], v[176:179], v[72:75]
	v_mfma_f32_16x16x32_bf16 v[68:71], v[148:151], v[172:175], 0
	v_mfma_f32_16x16x32_bf16 v[68:71], v[144:147], v[168:171], v[68:71]
	v_mfma_f32_16x16x32_bf16 v[64:67], v[140:143], v[172:175], 0
	v_mfma_f32_16x16x32_bf16 v[64:67], v[136:139], v[168:171], v[64:67]
	s_setprio 0
	s_barrier
	s_mov_b32 m0, s47
	s_mov_b32 s10, s14
	s_mov_b32 s11, s15
	buffer_load_dwordx4 v214, s[8:11], s43 offen lds
	s_add_i32 s43, s42, 0x40100
	s_mov_b32 m0, s62
	s_and_b64 vcc, exec, s[4:5]
	buffer_load_dwordx4 v214, s[8:11], s43 offen lds
	s_add_i32 s43, s42, 0x4100
	s_mov_b32 m0, s63
	s_nop 0
	buffer_load_dwordx4 v214, s[8:11], s43 offen lds
	s_add_i32 s43, s42, 0x44100
	s_mov_b32 m0, s64
	s_nop 0
	buffer_load_dwordx4 v214, s[8:11], s43 offen lds
	s_mov_b32 m0, s46
	s_add_i32 s10, s60, 0x80100
	buffer_load_dwordx4 v213, s[12:15], s33 offen lds
	s_mov_b32 m0, s65
	s_nop 0
	buffer_load_dwordx4 v213, s[12:15], s10 offen lds
	ds_read_b128 v[196:199], v232 offset:16384
	ds_read_b128 v[192:195], v232 offset:17408
	ds_read_b128 v[188:191], v232 offset:18432
	ds_read_b128 v[184:187], v232 offset:19456
	ds_read_b128 v[180:183], v232 offset:20480
	ds_read_b128 v[176:179], v232 offset:21504
	ds_read_b128 v[172:175], v232 offset:22528
	ds_read_b128 v[168:171], v232 offset:23552
	s_cbranch_vccz .LBB0_607
	s_waitcnt vmcnt(26)
	s_cbranch_execnz .LBB0_592

.LBB0_592:
	s_waitcnt lgkmcnt(0)
	s_add_i32 s4, s60, 0x180
	s_add_i32 s5, s42, 0x180
	s_barrier
	s_setprio 1
	s_waitcnt lgkmcnt(6)
	v_mfma_f32_16x16x32_bf16 v[60:63], v[164:167], v[196:199], 0
	v_mfma_f32_16x16x32_bf16 v[60:63], v[160:163], v[192:195], v[60:63]
	v_mfma_f32_16x16x32_bf16 v[56:59], v[156:159], v[196:199], 0
	v_mfma_f32_16x16x32_bf16 v[56:59], v[152:155], v[192:195], v[56:59]
	s_waitcnt lgkmcnt(4)
	v_mfma_f32_16x16x32_bf16 v[52:55], v[164:167], v[188:191], 0
	v_mfma_f32_16x16x32_bf16 v[52:55], v[160:163], v[184:187], v[52:55]
	v_mfma_f32_16x16x32_bf16 v[48:51], v[156:159], v[188:191], 0
	v_mfma_f32_16x16x32_bf16 v[48:51], v[152:155], v[184:187], v[48:51]
	s_waitcnt lgkmcnt(2)
	v_mfma_f32_16x16x32_bf16 v[44:47], v[164:167], v[180:183], 0
	v_mfma_f32_16x16x32_bf16 v[44:47], v[160:163], v[176:179], v[44:47]
	v_mfma_f32_16x16x32_bf16 v[40:43], v[156:159], v[180:183], 0
	v_mfma_f32_16x16x32_bf16 v[40:43], v[152:155], v[176:179], v[40:43]
	s_waitcnt lgkmcnt(0)
	v_mfma_f32_16x16x32_bf16 v[36:39], v[164:167], v[172:175], 0
	v_mfma_f32_16x16x32_bf16 v[36:39], v[160:163], v[168:171], v[36:39]
	v_mfma_f32_16x16x32_bf16 v[32:35], v[156:159], v[172:175], 0
	v_mfma_f32_16x16x32_bf16 v[32:35], v[152:155], v[168:171], v[32:35]
	s_setprio 0
	s_setprio 1
	v_mfma_f32_16x16x32_bf16 v[28:31], v[148:151], v[196:199], 0
	v_mfma_f32_16x16x32_bf16 v[28:31], v[144:147], v[192:195], v[28:31]
	v_mfma_f32_16x16x32_bf16 v[24:27], v[140:143], v[196:199], 0
	v_mfma_f32_16x16x32_bf16 v[24:27], v[136:139], v[192:195], v[24:27]
	v_mfma_f32_16x16x32_bf16 v[20:23], v[148:151], v[188:191], 0
	v_mfma_f32_16x16x32_bf16 v[20:23], v[144:147], v[184:187], v[20:23]
	v_mfma_f32_16x16x32_bf16 v[16:19], v[140:143], v[188:191], 0
	v_mfma_f32_16x16x32_bf16 v[16:19], v[136:139], v[184:187], v[16:19]
	v_mfma_f32_16x16x32_bf16 v[12:15], v[148:151], v[180:183], 0
	v_mfma_f32_16x16x32_bf16 v[12:15], v[144:147], v[176:179], v[12:15]
	v_mfma_f32_16x16x32_bf16 v[8:11], v[140:143], v[180:183], 0
	v_mfma_f32_16x16x32_bf16 v[8:11], v[136:139], v[176:179], v[8:11]
	v_mfma_f32_16x16x32_bf16 v[4:7], v[148:151], v[172:175], 0
	v_mfma_f32_16x16x32_bf16 v[4:7], v[144:147], v[168:171], v[4:7]
	v_mfma_f32_16x16x32_bf16 v[0:3], v[140:143], v[172:175], 0
	v_mfma_f32_16x16x32_bf16 v[0:3], v[136:139], v[168:171], v[0:3]
	s_setprio 0
	s_barrier
	ds_read_b128 v[164:167], v224
	ds_read_b128 v[160:163], v225
	ds_read_b128 v[156:159], v226
	ds_read_b128 v[152:155], v227
	ds_read_b128 v[148:151], v228
	ds_read_b128 v[144:147], v229
	ds_read_b128 v[140:143], v230
	ds_read_b128 v[136:139], v231
	ds_read_b128 v[168:171], v232 offset:32768
	ds_read_b128 v[172:175], v232 offset:33792
	ds_read_b128 v[176:179], v232 offset:34816
	ds_read_b128 v[180:183], v232 offset:35840
	ds_read_b128 v[184:187], v232 offset:36864
	ds_read_b128 v[188:191], v232 offset:37888
	ds_read_b128 v[192:195], v232 offset:38912
	ds_read_b128 v[196:199], v232 offset:39936
	s_mov_b32 m0, s68
	s_add_i32 s10, s60, 0x100100
	buffer_load_dwordx4 v213, s[12:15], s10 offen lds
	s_add_i32 s10, s60, 0x180100
	s_mov_b32 m0, s69
	s_nop 0
	buffer_load_dwordx4 v213, s[12:15], s10 offen lds
	s_waitcnt vmcnt(10)
	s_waitcnt lgkmcnt(8)
	s_barrier
	s_setprio 1
	s_waitcnt lgkmcnt(6)
	v_mfma_f32_16x16x32_bf16 v[124:127], v[164:167], v[168:171], v[124:127]
	v_mfma_f32_16x16x32_bf16 v[124:127], v[160:163], v[172:175], v[124:127]
	v_mfma_f32_16x16x32_bf16 v[120:123], v[156:159], v[168:171], v[120:123]
	v_mfma_f32_16x16x32_bf16 v[120:123], v[152:155], v[172:175], v[120:123]
	s_waitcnt lgkmcnt(4)
	v_mfma_f32_16x16x32_bf16 v[116:119], v[164:167], v[176:179], v[116:119]
	v_mfma_f32_16x16x32_bf16 v[116:119], v[160:163], v[180:183], v[116:119]
	v_mfma_f32_16x16x32_bf16 v[112:115], v[156:159], v[176:179], v[112:115]
	v_mfma_f32_16x16x32_bf16 v[112:115], v[152:155], v[180:183], v[112:115]
	s_waitcnt lgkmcnt(2)
	v_mfma_f32_16x16x32_bf16 v[108:111], v[164:167], v[184:187], v[108:111]
	v_mfma_f32_16x16x32_bf16 v[108:111], v[160:163], v[188:191], v[108:111]
	v_mfma_f32_16x16x32_bf16 v[104:107], v[156:159], v[184:187], v[104:107]
	v_mfma_f32_16x16x32_bf16 v[104:107], v[152:155], v[188:191], v[104:107]
	s_waitcnt lgkmcnt(0)
	v_mfma_f32_16x16x32_bf16 v[100:103], v[164:167], v[192:195], v[100:103]
	v_mfma_f32_16x16x32_bf16 v[100:103], v[160:163], v[196:199], v[100:103]
	v_mfma_f32_16x16x32_bf16 v[96:99], v[156:159], v[192:195], v[96:99]
	v_mfma_f32_16x16x32_bf16 v[96:99], v[152:155], v[196:199], v[96:99]
	s_setprio 0
	s_setprio 1
	v_mfma_f32_16x16x32_bf16 v[92:95], v[148:151], v[168:171], v[92:95]
	v_mfma_f32_16x16x32_bf16 v[92:95], v[144:147], v[172:175], v[92:95]
	v_mfma_f32_16x16x32_bf16 v[88:91], v[140:143], v[168:171], v[88:91]
	v_mfma_f32_16x16x32_bf16 v[88:91], v[136:139], v[172:175], v[88:91]
	v_mfma_f32_16x16x32_bf16 v[84:87], v[148:151], v[176:179], v[84:87]
	v_mfma_f32_16x16x32_bf16 v[84:87], v[144:147], v[180:183], v[84:87]
	v_mfma_f32_16x16x32_bf16 v[80:83], v[140:143], v[176:179], v[80:83]
	v_mfma_f32_16x16x32_bf16 v[80:83], v[136:139], v[180:183], v[80:83]
	v_mfma_f32_16x16x32_bf16 v[76:79], v[148:151], v[184:187], v[76:79]
	v_mfma_f32_16x16x32_bf16 v[76:79], v[144:147], v[188:191], v[76:79]
	v_mfma_f32_16x16x32_bf16 v[72:75], v[140:143], v[184:187], v[72:75]
	v_mfma_f32_16x16x32_bf16 v[72:75], v[136:139], v[188:191], v[72:75]
	v_mfma_f32_16x16x32_bf16 v[68:71], v[148:151], v[192:195], v[68:71]
	v_mfma_f32_16x16x32_bf16 v[68:71], v[144:147], v[196:199], v[68:71]
	v_mfma_f32_16x16x32_bf16 v[64:67], v[140:143], v[192:195], v[64:67]
	v_mfma_f32_16x16x32_bf16 v[64:67], v[136:139], v[196:199], v[64:67]
	s_setprio 0
	s_barrier
	ds_read_b128 v[168:171], v232 offset:49152
	ds_read_b128 v[172:175], v232 offset:50176
	ds_read_b128 v[176:179], v232 offset:51200
	ds_read_b128 v[180:183], v232 offset:52224
	ds_read_b128 v[184:187], v232 offset:53248
	ds_read_b128 v[188:191], v232 offset:54272
	ds_read_b128 v[192:195], v232 offset:55296
	ds_read_b128 v[196:199], v232 offset:56320
	s_mov_b32 m0, s72
	s_mov_b32 s10, s14
	s_mov_b32 s11, s15
	buffer_load_dwordx4 v214, s[8:11], s5 offen lds
	s_add_i32 s5, s42, 0x40180
	s_mov_b32 m0, s73
	s_nop 0
	buffer_load_dwordx4 v214, s[8:11], s5 offen lds
	s_add_i32 s5, s42, 0x4180
	s_mov_b32 m0, s76
	s_nop 0
	buffer_load_dwordx4 v214, s[8:11], s5 offen lds
	s_add_i32 s5, s42, 0x44180
	s_mov_b32 m0, s77
	s_nop 0
	buffer_load_dwordx4 v214, s[8:11], s5 offen lds
	s_mov_b32 m0, s74
	s_nop 0
	buffer_load_dwordx4 v213, s[12:15], s4 offen lds
	s_add_i32 s4, s60, 0x80180
	s_mov_b32 m0, s75
	s_nop 0
	buffer_load_dwordx4 v213, s[12:15], s4 offen lds
	s_waitcnt vmcnt(8)
	s_waitcnt lgkmcnt(6)
	s_barrier
	s_setprio 1
	s_waitcnt lgkmcnt(6)
	v_mfma_f32_16x16x32_bf16 v[60:63], v[164:167], v[168:171], v[60:63]
	v_mfma_f32_16x16x32_bf16 v[60:63], v[160:163], v[172:175], v[60:63]
	v_mfma_f32_16x16x32_bf16 v[56:59], v[156:159], v[168:171], v[56:59]
	v_mfma_f32_16x16x32_bf16 v[56:59], v[152:155], v[172:175], v[56:59]
	s_waitcnt lgkmcnt(4)
	v_mfma_f32_16x16x32_bf16 v[52:55], v[164:167], v[176:179], v[52:55]
	v_mfma_f32_16x16x32_bf16 v[52:55], v[160:163], v[180:183], v[52:55]
	v_mfma_f32_16x16x32_bf16 v[48:51], v[156:159], v[176:179], v[48:51]
	v_mfma_f32_16x16x32_bf16 v[48:51], v[152:155], v[180:183], v[48:51]
	s_waitcnt lgkmcnt(2)
	v_mfma_f32_16x16x32_bf16 v[44:47], v[164:167], v[184:187], v[44:47]
	v_mfma_f32_16x16x32_bf16 v[44:47], v[160:163], v[188:191], v[44:47]
	v_mfma_f32_16x16x32_bf16 v[40:43], v[156:159], v[184:187], v[40:43]
	v_mfma_f32_16x16x32_bf16 v[40:43], v[152:155], v[188:191], v[40:43]
	s_waitcnt lgkmcnt(0)
	v_mfma_f32_16x16x32_bf16 v[36:39], v[164:167], v[192:195], v[36:39]
	v_mfma_f32_16x16x32_bf16 v[36:39], v[160:163], v[196:199], v[36:39]
	v_mfma_f32_16x16x32_bf16 v[32:35], v[156:159], v[192:195], v[32:35]
	v_mfma_f32_16x16x32_bf16 v[32:35], v[152:155], v[196:199], v[32:35]
	s_setprio 0
	s_setprio 1
	v_mfma_f32_16x16x32_bf16 v[28:31], v[148:151], v[168:171], v[28:31]
	v_mfma_f32_16x16x32_bf16 v[28:31], v[144:147], v[172:175], v[28:31]
	v_mfma_f32_16x16x32_bf16 v[24:27], v[140:143], v[168:171], v[24:27]
	v_mfma_f32_16x16x32_bf16 v[24:27], v[136:139], v[172:175], v[24:27]
	v_mfma_f32_16x16x32_bf16 v[20:23], v[148:151], v[176:179], v[20:23]
	v_mfma_f32_16x16x32_bf16 v[20:23], v[144:147], v[180:183], v[20:23]
	v_mfma_f32_16x16x32_bf16 v[16:19], v[140:143], v[176:179], v[16:19]
	v_mfma_f32_16x16x32_bf16 v[16:19], v[136:139], v[180:183], v[16:19]
	v_mfma_f32_16x16x32_bf16 v[12:15], v[148:151], v[184:187], v[12:15]
	v_mfma_f32_16x16x32_bf16 v[12:15], v[144:147], v[188:191], v[12:15]
	v_mfma_f32_16x16x32_bf16 v[8:11], v[140:143], v[184:187], v[8:11]
	v_mfma_f32_16x16x32_bf16 v[8:11], v[136:139], v[188:191], v[8:11]
	v_mfma_f32_16x16x32_bf16 v[4:7], v[148:151], v[192:195], v[4:7]
	v_mfma_f32_16x16x32_bf16 v[4:7], v[144:147], v[196:199], v[4:7]
	v_mfma_f32_16x16x32_bf16 v[0:3], v[140:143], v[192:195], v[0:3]
	v_mfma_f32_16x16x32_bf16 v[0:3], v[136:139], v[196:199], v[0:3]
	s_setprio 0
	s_barrier
	s_waitcnt vmcnt(14)
	v_mul_f32_e32 v132, 0x42800000, v132
	v_mul_f32_e32 v128, 0x42800000, v128
	v_mul_f32_e32 v133, 0x42800000, v133
	v_mul_f32_e32 v129, 0x42800000, v129
	v_mul_f32_e32 v134, 0x42800000, v134
	v_mul_f32_e32 v130, 0x42800000, v130
	v_mul_f32_e32 v135, 0x42800000, v135
	v_mul_f32_e32 v131, 0x42800000, v131
	v_cvt_pk_fp8_f32 v202, v128, v132
	v_cvt_pk_fp8_f32 v233, v129, v133
	v_cvt_pk_fp8_f32 v234, v130, v134
	v_cvt_pk_fp8_f32 v235, v131, v135
	s_add_i32 s33, s42, 0x200
	s_mov_b32 s66, 0
	s_mov_b32 s89, s70
	s_mov_b32 s90, s71
	s_branch .LBB0_595

.LBB0_595:
	v_mov_b32_e32 v152, v202
	v_mov_b32_e32 v153, v233
	v_mov_b32_e32 v154, v234
	v_mov_b32_e32 v155, v235
	ds_read_b128 v[158:161], v216
	ds_read_b128 v[162:165], v217
	ds_read_b128 v[166:169], v218
	ds_read_b128 v[170:173], v219
	ds_read_b128 v[148:151], v220
	ds_read_b128 v[144:147], v221
	ds_read_b128 v[140:143], v222
	ds_read_b128 v[136:139], v223
	ds_read_b128 v[174:177], v232
	ds_read_b128 v[178:181], v232 offset:1024
	ds_read_b128 v[182:185], v232 offset:2048
	ds_read_b128 v[186:189], v232 offset:3072
	ds_read_b128 v[190:193], v232 offset:4096
	ds_read_b128 v[194:197], v232 offset:5120
	ds_read_b128 v[234:237], v232 offset:6144
	ds_read_b128 v[238:241], v232 offset:7168
	s_add_i32 s4, s60, s66
	s_mov_b32 s42, s90
	s_add_i32 s90, s90, 1
	s_add_i32 s5, s4, 0x200
	s_add_i32 s67, s33, s66
	s_cmpk_eq_i32 s66, 0x200
	s_cselect_b32 s43, s87, s5
	s_cselect_b32 s93, s88, s67
	s_add_i32 s92, s43, 0x80
	s_mov_b32 m0, s78
	s_add_i32 s5, s4, 0x100180
	buffer_load_dwordx4 v213, s[12:15], s5 offen lds
	s_add_i32 s4, s4, 0x180180
	s_mov_b32 m0, s81
	s_add_i32 s94, s93, 0x80
	buffer_load_dwordx4 v213, s[12:15], s4 offen lds
	s_lshr_b32 s4, s90, 2
	s_mul_i32 s67, s4, s34
	s_add_i32 s67, s67, s2
	s_cmp_lt_i32 s4, s3
	s_cselect_b64 s[4:5], -1, 0
	s_and_b64 s[96:97], s[4:5], exec
	s_cselect_b32 s91, s67, 0
	s_ashr_i32 s96, s91, 7
	s_bfe_u32 s95, s90, 0x10001
	s_ashr_i32 s97, s96, 31
	s_or_b32 s95, s95, s79
	s_lshl_b64 s[96:97], s[96:97], 23
	s_add_u32 s96, s48, s96
	s_addc_u32 s97, s49, s97
	s_lshl_b32 vcc_lo, s91, 16
	s_and_b32 vcc_lo, vcc_lo, 0x600000
	s_add_u32 s96, s96, vcc_lo
	s_addc_u32 s97, s97, 0
	s_lshl_b32 s91, s91, 7
	s_and_b32 s91, s91, 0xf80
	s_lshl_b32 vcc_lo, s91, 2
	s_add_u32 s96, s96, vcc_lo
	v_and_or_b32 v202, s89, 2, v200
	s_addc_u32 s97, s97, 0
	v_lshl_or_b32 v156, s95, 5, v215
	v_lshlrev_b64 v[128:129], 14, v[202:203]
	v_lshl_add_u64 v[128:129], s[96:97], 0, v[128:129]
	v_lshlrev_b32_e32 v202, 2, v156
	v_lshl_add_u64 v[128:129], v[128:129], 0, v[202:203]
	s_movk_i32 s95, 0x4000
	v_add_co_u32_e32 v132, vcc, s95, v128
	s_nop 1
	v_addc_co_u32_e32 v133, vcc, 0, v129, vcc
	global_load_dwordx4 v[128:131], v[128:129], off nt
	s_nop 0
	global_load_dwordx4 v[132:135], v[132:133], off nt
	s_waitcnt vmcnt(10)
	s_waitcnt lgkmcnt(8)
	s_barrier
	s_setprio 1
	s_waitcnt lgkmcnt(6)
	v_mfma_f32_16x16x32_bf16 v[124:127], v[158:161], v[174:177], v[124:127]
	v_mfma_f32_16x16x32_bf16 v[124:127], v[162:165], v[178:181], v[124:127]
	v_mfma_f32_16x16x32_bf16 v[120:123], v[166:169], v[174:177], v[120:123]
	v_mfma_f32_16x16x32_bf16 v[120:123], v[170:173], v[178:181], v[120:123]
	s_waitcnt lgkmcnt(4)
	v_mfma_f32_16x16x32_bf16 v[116:119], v[158:161], v[182:185], v[116:119]
	v_mfma_f32_16x16x32_bf16 v[116:119], v[162:165], v[186:189], v[116:119]
	v_mfma_f32_16x16x32_bf16 v[112:115], v[166:169], v[182:185], v[112:115]
	v_mfma_f32_16x16x32_bf16 v[112:115], v[170:173], v[186:189], v[112:115]
	s_waitcnt lgkmcnt(2)
	v_mfma_f32_16x16x32_bf16 v[108:111], v[158:161], v[190:193], v[108:111]
	v_mfma_f32_16x16x32_bf16 v[108:111], v[162:165], v[194:197], v[108:111]
	v_mfma_f32_16x16x32_bf16 v[104:107], v[166:169], v[190:193], v[104:107]
	v_mfma_f32_16x16x32_bf16 v[104:107], v[170:173], v[194:197], v[104:107]
	s_waitcnt lgkmcnt(0)
	v_mfma_f32_16x16x32_bf16 v[100:103], v[158:161], v[234:237], v[100:103]
	v_mfma_f32_16x16x32_bf16 v[100:103], v[162:165], v[238:241], v[100:103]
	v_mfma_f32_16x16x32_bf16 v[96:99], v[166:169], v[234:237], v[96:99]
	v_mfma_f32_16x16x32_bf16 v[96:99], v[170:173], v[238:241], v[96:99]
	s_setprio 0
	s_setprio 1
	v_mfma_f32_16x16x32_bf16 v[92:95], v[148:151], v[174:177], v[92:95]
	v_mfma_f32_16x16x32_bf16 v[92:95], v[144:147], v[178:181], v[92:95]
	v_mfma_f32_16x16x32_bf16 v[88:91], v[140:143], v[174:177], v[88:91]
	v_mfma_f32_16x16x32_bf16 v[88:91], v[136:139], v[178:181], v[88:91]
	v_mfma_f32_16x16x32_bf16 v[84:87], v[148:151], v[182:185], v[84:87]
	v_mfma_f32_16x16x32_bf16 v[84:87], v[144:147], v[186:189], v[84:87]
	v_mfma_f32_16x16x32_bf16 v[80:83], v[140:143], v[182:185], v[80:83]
	v_mfma_f32_16x16x32_bf16 v[80:83], v[136:139], v[186:189], v[80:83]
	v_mfma_f32_16x16x32_bf16 v[76:79], v[148:151], v[190:193], v[76:79]
	v_mfma_f32_16x16x32_bf16 v[76:79], v[144:147], v[194:197], v[76:79]
	v_mfma_f32_16x16x32_bf16 v[72:75], v[140:143], v[190:193], v[72:75]
	v_mfma_f32_16x16x32_bf16 v[72:75], v[136:139], v[194:197], v[72:75]
	v_mfma_f32_16x16x32_bf16 v[68:71], v[148:151], v[234:237], v[68:71]
	v_mfma_f32_16x16x32_bf16 v[68:71], v[144:147], v[238:241], v[68:71]
	v_mfma_f32_16x16x32_bf16 v[64:67], v[140:143], v[234:237], v[64:67]
	v_mfma_f32_16x16x32_bf16 v[64:67], v[136:139], v[238:241], v[64:67]
	s_setprio 0
	s_barrier
	ds_read_b128 v[174:177], v232 offset:16384
	ds_read_b128 v[178:181], v232 offset:17408
	ds_read_b128 v[182:185], v232 offset:18432
	ds_read_b128 v[186:189], v232 offset:19456
	ds_read_b128 v[190:193], v232 offset:20480
	ds_read_b128 v[194:197], v232 offset:21504
	ds_read_b128 v[234:237], v232 offset:22528
	ds_read_b128 v[238:241], v232 offset:23552
	s_mov_b32 m0, s47
	s_add_i32 s95, s93, 0x40000
	buffer_load_dwordx4 v214, s[8:11], s93 offen lds
	s_mov_b32 m0, s62
	s_nop 0
	buffer_load_dwordx4 v214, s[8:11], s95 offen lds
	s_add_i32 s95, s93, 0x4000
	s_mov_b32 m0, s63
	s_nop 0
	buffer_load_dwordx4 v214, s[8:11], s95 offen lds
	s_add_i32 s95, s93, 0x44000
	s_mov_b32 m0, s64
	s_nop 0
	buffer_load_dwordx4 v214, s[8:11], s95 offen lds
	s_mov_b32 m0, s46
	s_add_i32 s95, s43, 0x80000
	buffer_load_dwordx4 v213, s[12:15], s43 offen lds
	s_mov_b32 m0, s65
	s_nop 0
	buffer_load_dwordx4 v213, s[12:15], s95 offen lds
	s_waitcnt vmcnt(10)
	s_waitcnt lgkmcnt(6)
	s_barrier
	s_setprio 1
	s_waitcnt lgkmcnt(6)
	v_mfma_f32_16x16x32_bf16 v[60:63], v[158:161], v[174:177], v[60:63]
	v_mfma_f32_16x16x32_bf16 v[60:63], v[162:165], v[178:181], v[60:63]
	v_mfma_f32_16x16x32_bf16 v[56:59], v[166:169], v[174:177], v[56:59]
	v_mfma_f32_16x16x32_bf16 v[56:59], v[170:173], v[178:181], v[56:59]
	s_waitcnt lgkmcnt(4)
	v_mfma_f32_16x16x32_bf16 v[52:55], v[158:161], v[182:185], v[52:55]
	v_mfma_f32_16x16x32_bf16 v[52:55], v[162:165], v[186:189], v[52:55]
	v_mfma_f32_16x16x32_bf16 v[48:51], v[166:169], v[182:185], v[48:51]
	v_mfma_f32_16x16x32_bf16 v[48:51], v[170:173], v[186:189], v[48:51]
	s_waitcnt lgkmcnt(2)
	v_mfma_f32_16x16x32_bf16 v[44:47], v[158:161], v[190:193], v[44:47]
	v_mfma_f32_16x16x32_bf16 v[44:47], v[162:165], v[194:197], v[44:47]
	v_mfma_f32_16x16x32_bf16 v[40:43], v[166:169], v[190:193], v[40:43]
	v_mfma_f32_16x16x32_bf16 v[40:43], v[170:173], v[194:197], v[40:43]
	s_waitcnt lgkmcnt(0)
	v_mfma_f32_16x16x32_bf16 v[36:39], v[158:161], v[234:237], v[36:39]
	v_mfma_f32_16x16x32_bf16 v[36:39], v[162:165], v[238:241], v[36:39]
	v_mfma_f32_16x16x32_bf16 v[32:35], v[166:169], v[234:237], v[32:35]
	v_mfma_f32_16x16x32_bf16 v[32:35], v[170:173], v[238:241], v[32:35]
	s_setprio 0
	s_setprio 1
	v_mfma_f32_16x16x32_bf16 v[28:31], v[148:151], v[174:177], v[28:31]
	v_mfma_f32_16x16x32_bf16 v[28:31], v[144:147], v[178:181], v[28:31]
	v_mfma_f32_16x16x32_bf16 v[24:27], v[140:143], v[174:177], v[24:27]
	v_mfma_f32_16x16x32_bf16 v[24:27], v[136:139], v[178:181], v[24:27]
	v_mfma_f32_16x16x32_bf16 v[20:23], v[148:151], v[182:185], v[20:23]
	v_mfma_f32_16x16x32_bf16 v[20:23], v[144:147], v[186:189], v[20:23]
	v_mfma_f32_16x16x32_bf16 v[16:19], v[140:143], v[182:185], v[16:19]
	v_mfma_f32_16x16x32_bf16 v[16:19], v[136:139], v[186:189], v[16:19]
	v_mfma_f32_16x16x32_bf16 v[12:15], v[148:151], v[190:193], v[12:15]
	v_mfma_f32_16x16x32_bf16 v[12:15], v[144:147], v[194:197], v[12:15]
	v_mfma_f32_16x16x32_bf16 v[8:11], v[140:143], v[190:193], v[8:11]
	v_mfma_f32_16x16x32_bf16 v[8:11], v[136:139], v[194:197], v[8:11]
	v_mfma_f32_16x16x32_bf16 v[4:7], v[148:151], v[234:237], v[4:7]
	v_mfma_f32_16x16x32_bf16 v[4:7], v[144:147], v[238:241], v[4:7]
	v_mfma_f32_16x16x32_bf16 v[0:3], v[140:143], v[234:237], v[0:3]
	v_mfma_f32_16x16x32_bf16 v[0:3], v[136:139], v[238:241], v[0:3]
	s_setprio 0
	s_barrier
	ds_read_b128 v[136:139], v224
	ds_read_b128 v[140:143], v225
	ds_read_b128 v[144:147], v226
	ds_read_b128 v[148:151], v227
	ds_read_b128 v[158:161], v228
	ds_read_b128 v[162:165], v229
	ds_read_b128 v[166:169], v230
	ds_read_b128 v[170:173], v231
	ds_read_b128 v[174:177], v232 offset:32768
	ds_read_b128 v[178:181], v232 offset:33792
	ds_read_b128 v[182:185], v232 offset:34816
	ds_read_b128 v[186:189], v232 offset:35840
	ds_read_b128 v[190:193], v232 offset:36864
	ds_read_b128 v[194:197], v232 offset:37888
	ds_read_b128 v[234:237], v232 offset:38912
	ds_read_b128 v[238:241], v232 offset:39936
	s_mov_b32 m0, s68
	s_add_i32 s95, s43, 0x100000
	buffer_load_dwordx4 v213, s[12:15], s95 offen lds
	s_add_i32 s95, s43, 0x180000
	s_mov_b32 m0, s69
	s_nop 0
	buffer_load_dwordx4 v213, s[12:15], s95 offen lds
	s_waitcnt vmcnt(10)
	s_waitcnt lgkmcnt(8)
	s_barrier
	s_setprio 1
	s_waitcnt lgkmcnt(6)
	v_mfma_f32_16x16x32_bf16 v[124:127], v[136:139], v[174:177], v[124:127]
	v_mfma_f32_16x16x32_bf16 v[124:127], v[140:143], v[178:181], v[124:127]
	v_mfma_f32_16x16x32_bf16 v[120:123], v[144:147], v[174:177], v[120:123]
	v_mfma_f32_16x16x32_bf16 v[120:123], v[148:151], v[178:181], v[120:123]
	s_waitcnt lgkmcnt(4)
	v_mfma_f32_16x16x32_bf16 v[116:119], v[136:139], v[182:185], v[116:119]
	v_mfma_f32_16x16x32_bf16 v[116:119], v[140:143], v[186:189], v[116:119]
	v_mfma_f32_16x16x32_bf16 v[112:115], v[144:147], v[182:185], v[112:115]
	v_mfma_f32_16x16x32_bf16 v[112:115], v[148:151], v[186:189], v[112:115]
	s_waitcnt lgkmcnt(2)
	v_mfma_f32_16x16x32_bf16 v[108:111], v[136:139], v[190:193], v[108:111]
	v_mfma_f32_16x16x32_bf16 v[108:111], v[140:143], v[194:197], v[108:111]
	v_mfma_f32_16x16x32_bf16 v[104:107], v[144:147], v[190:193], v[104:107]
	v_mfma_f32_16x16x32_bf16 v[104:107], v[148:151], v[194:197], v[104:107]
	s_waitcnt lgkmcnt(0)
	v_mfma_f32_16x16x32_bf16 v[100:103], v[136:139], v[234:237], v[100:103]
	v_mfma_f32_16x16x32_bf16 v[100:103], v[140:143], v[238:241], v[100:103]
	v_mfma_f32_16x16x32_bf16 v[96:99], v[144:147], v[234:237], v[96:99]
	v_mfma_f32_16x16x32_bf16 v[96:99], v[148:151], v[238:241], v[96:99]
	s_setprio 0
	s_setprio 1
	v_mfma_f32_16x16x32_bf16 v[92:95], v[158:161], v[174:177], v[92:95]
	v_mfma_f32_16x16x32_bf16 v[92:95], v[162:165], v[178:181], v[92:95]
	v_mfma_f32_16x16x32_bf16 v[88:91], v[166:169], v[174:177], v[88:91]
	v_mfma_f32_16x16x32_bf16 v[88:91], v[170:173], v[178:181], v[88:91]
	v_mfma_f32_16x16x32_bf16 v[84:87], v[158:161], v[182:185], v[84:87]
	v_mfma_f32_16x16x32_bf16 v[84:87], v[162:165], v[186:189], v[84:87]
	v_mfma_f32_16x16x32_bf16 v[80:83], v[166:169], v[182:185], v[80:83]
	v_mfma_f32_16x16x32_bf16 v[80:83], v[170:173], v[186:189], v[80:83]
	v_mfma_f32_16x16x32_bf16 v[76:79], v[158:161], v[190:193], v[76:79]
	v_mfma_f32_16x16x32_bf16 v[76:79], v[162:165], v[194:197], v[76:79]
	v_mfma_f32_16x16x32_bf16 v[72:75], v[166:169], v[190:193], v[72:75]
	v_mfma_f32_16x16x32_bf16 v[72:75], v[170:173], v[194:197], v[72:75]
	v_mfma_f32_16x16x32_bf16 v[68:71], v[158:161], v[234:237], v[68:71]
	v_mfma_f32_16x16x32_bf16 v[68:71], v[162:165], v[238:241], v[68:71]
	v_mfma_f32_16x16x32_bf16 v[64:67], v[166:169], v[234:237], v[64:67]
	v_mfma_f32_16x16x32_bf16 v[64:67], v[170:173], v[238:241], v[64:67]
	s_setprio 0
	s_barrier
	ds_read_b128 v[174:177], v232 offset:49152
	ds_read_b128 v[178:181], v232 offset:50176
	ds_read_b128 v[182:185], v232 offset:51200
	ds_read_b128 v[186:189], v232 offset:52224
	ds_read_b128 v[190:193], v232 offset:53248
	ds_read_b128 v[194:197], v232 offset:54272
	ds_read_b128 v[234:237], v232 offset:55296
	ds_read_b128 v[238:241], v232 offset:56320
	s_mov_b32 m0, s72
	s_add_i32 s43, s43, 0x80080
	buffer_load_dwordx4 v214, s[8:11], s94 offen lds
	s_add_i32 s94, s93, 0x40080
	s_mov_b32 m0, s73
	s_nop 0
	buffer_load_dwordx4 v214, s[8:11], s94 offen lds
	s_add_i32 s94, s93, 0x4080
	s_mov_b32 m0, s76
	s_add_i32 s93, s93, 0x44080
	buffer_load_dwordx4 v214, s[8:11], s94 offen lds
	s_mov_b32 m0, s77
	s_nop 0
	buffer_load_dwordx4 v214, s[8:11], s93 offen lds
	s_mov_b32 m0, s74
	s_nop 0
	buffer_load_dwordx4 v213, s[12:15], s92 offen lds
	s_mov_b32 m0, s75
	s_nop 0
	buffer_load_dwordx4 v213, s[12:15], s43 offen lds
	s_waitcnt vmcnt(8)
	s_waitcnt lgkmcnt(6)
	s_barrier
	s_setprio 1
	s_waitcnt lgkmcnt(6)
	v_mfma_f32_16x16x32_bf16 v[60:63], v[136:139], v[174:177], v[60:63]
	v_mfma_f32_16x16x32_bf16 v[60:63], v[140:143], v[178:181], v[60:63]
	v_mfma_f32_16x16x32_bf16 v[56:59], v[144:147], v[174:177], v[56:59]
	v_mfma_f32_16x16x32_bf16 v[56:59], v[148:151], v[178:181], v[56:59]
	s_waitcnt lgkmcnt(4)
	v_mfma_f32_16x16x32_bf16 v[52:55], v[136:139], v[182:185], v[52:55]
	v_mfma_f32_16x16x32_bf16 v[52:55], v[140:143], v[186:189], v[52:55]
	v_mfma_f32_16x16x32_bf16 v[48:51], v[144:147], v[182:185], v[48:51]
	v_mfma_f32_16x16x32_bf16 v[48:51], v[148:151], v[186:189], v[48:51]
	s_waitcnt lgkmcnt(2)
	v_mfma_f32_16x16x32_bf16 v[44:47], v[136:139], v[190:193], v[44:47]
	v_mfma_f32_16x16x32_bf16 v[44:47], v[140:143], v[194:197], v[44:47]
	v_mfma_f32_16x16x32_bf16 v[40:43], v[144:147], v[190:193], v[40:43]
	v_mfma_f32_16x16x32_bf16 v[40:43], v[148:151], v[194:197], v[40:43]
	s_waitcnt lgkmcnt(0)
	v_mfma_f32_16x16x32_bf16 v[36:39], v[136:139], v[234:237], v[36:39]
	v_mfma_f32_16x16x32_bf16 v[36:39], v[140:143], v[238:241], v[36:39]
	v_mfma_f32_16x16x32_bf16 v[32:35], v[144:147], v[234:237], v[32:35]
	v_mfma_f32_16x16x32_bf16 v[32:35], v[148:151], v[238:241], v[32:35]
	s_setprio 0
	s_setprio 1
	v_mfma_f32_16x16x32_bf16 v[28:31], v[158:161], v[174:177], v[28:31]
	v_mfma_f32_16x16x32_bf16 v[28:31], v[162:165], v[178:181], v[28:31]
	v_mfma_f32_16x16x32_bf16 v[24:27], v[166:169], v[174:177], v[24:27]
	v_mfma_f32_16x16x32_bf16 v[24:27], v[170:173], v[178:181], v[24:27]
	v_mfma_f32_16x16x32_bf16 v[20:23], v[158:161], v[182:185], v[20:23]
	v_mfma_f32_16x16x32_bf16 v[20:23], v[162:165], v[186:189], v[20:23]
	v_mfma_f32_16x16x32_bf16 v[16:19], v[166:169], v[182:185], v[16:19]
	v_mfma_f32_16x16x32_bf16 v[16:19], v[170:173], v[186:189], v[16:19]
	v_mfma_f32_16x16x32_bf16 v[12:15], v[158:161], v[190:193], v[12:15]
	v_mfma_f32_16x16x32_bf16 v[12:15], v[162:165], v[194:197], v[12:15]
	v_mfma_f32_16x16x32_bf16 v[8:11], v[166:169], v[190:193], v[8:11]
	v_mfma_f32_16x16x32_bf16 v[8:11], v[170:173], v[194:197], v[8:11]
	v_mfma_f32_16x16x32_bf16 v[4:7], v[158:161], v[234:237], v[4:7]
	v_mfma_f32_16x16x32_bf16 v[4:7], v[162:165], v[238:241], v[4:7]
	v_mfma_f32_16x16x32_bf16 v[0:3], v[166:169], v[234:237], v[0:3]
	v_mfma_f32_16x16x32_bf16 v[0:3], v[170:173], v[238:241], v[0:3]
	s_setprio 0
	s_barrier
	s_bitcmp0_b32 s42, 0
	s_waitcnt vmcnt(15)
	v_mul_f32_e32 v128, 0x42800000, v128
	s_waitcnt vmcnt(14)
	v_mul_f32_e32 v132, 0x42800000, v132
	v_mul_f32_e32 v129, 0x42800000, v129
	v_mul_f32_e32 v133, 0x42800000, v133
	v_mul_f32_e32 v130, 0x42800000, v130
	v_mul_f32_e32 v134, 0x42800000, v134
	v_mul_f32_e32 v131, 0x42800000, v131
	v_mul_f32_e32 v135, 0x42800000, v135
	s_mov_b64 s[42:43], -1
	s_cbranch_scc0 .LBB0_598
	s_andn2_b64 vcc, exec, s[42:43]
	s_cbranch_vccnz .LBB0_594
	s_branch .LBB0_599
